# v64 plus two fewer VALU per attention step (dead row-max copy removed, row-sum chain start merged)
# baseline (speedup 1.0000x reference)
; template <bool FIRST>
; __device__ __forceinline__ void partialSM(f32x16& p0, f32x16& p1, float& m_reg, f32x16& nm16, float& alpha) {
;   float pmax = p0[0];
; #pragma unroll
;   for (int r = 1; r < 16; ++r) pmax = fmaxf(pmax, p0[r]);
; #pragma unroll
;   for (int r = 0; r < 16; ++r) pmax = fmaxf(pmax, p1[r]);
;   { auto rr = __builtin_amdgcn_permlane32_swap(__float_as_uint(pmax), __float_as_uint(pmax), false, false);
;     pmax = fmaxf(__uint_as_float(rr[0]), __uint_as_float(rr[1])); }
;   if (!FIRST && __builtin_expect(__all(pmax <= THR2), 1)) { alpha = 1.f; }
;   else { const float d = FIRST ? pmax : fmaxf(pmax, 0.f);
;     alpha = FIRST ? 1.f : __builtin_amdgcn_exp2f(-d); m_reg += d;
;     const float nm = -m_reg;
; #pragma unroll
;     for (int r = 0; r < 16; ++r) { p0[r] -= d; p1[r] -= d; float t = nm16[r]; asm volatile("v_mov_b32 %0, %1" : "+v"(t) : "v"(nm)); nm16[r] = t; } }
; #pragma unroll
;   for (int r = 0; r < 16; ++r) p0[r] = __builtin_amdgcn_exp2f(p0[r]);
; }
; __device__ __forceinline__ void finishSM(f32x16& p0, f32x16& p1, float alpha, float& l_reg, v8i& pa) {
; #pragma unroll
;   for (int r = 0; r < 16; ++r) p1[r] = __builtin_amdgcn_exp2f(p1[r]);
;   float ps = 0;
; #pragma unroll
;   for (int r = 0; r < 16; ++r) ps += p0[r];
; #pragma unroll
;   for (int r = 0; r < 16; ++r) ps += p1[r];
;   { auto rr = __builtin_amdgcn_permlane32_swap(__float_as_uint(ps), __float_as_uint(ps), false, false);
;     ps = __uint_as_float(rr[0]) + __uint_as_float(rr[1]); }
;   l_reg = l_reg * alpha + ps;
; #pragma unroll
;   for (int q = 0; q < 4; ++q) { int w0 = pa[q], w1 = pa[4 + q];
;     w0 = __builtin_amdgcn_cvt_pk_fp8_f32(p0[4 * q], p0[4 * q + 1], w0, false); w0 = __builtin_amdgcn_cvt_pk_fp8_f32(p0[4 * q + 2], p0[4 * q + 3], w0, true);
;     w1 = __builtin_amdgcn_cvt_pk_fp8_f32(p1[4 * q], p1[4 * q + 1], w1, false); w1 = __builtin_amdgcn_cvt_pk_fp8_f32(p1[4 * q + 2], p1[4 * q + 3], w1, true);
;     pa[q] = w0; pa[4 + q] = w1; }
; }
; __device__ __forceinline__ void qkt(f32x16& p0, f32x16& p1, const char* Ks, const v8i* qr, int r32, int hi, const f32x16& nm16) {
; #pragma unroll
;   for (int s = 0; s < 3; ++s) { const int c0 = 4 * s + 2 * hi;
;     const v8i a0 = __builtin_shufflevector(*reinterpret_cast<const v4i*>(Ks + k8_off(r32, c0)), *reinterpret_cast<const v4i*>(Ks + k8_off(r32, c0 + 1)), 0, 1, 2, 3, 4, 5, 6, 7);
.Lstg_top_l0:
	ds_read_b128 v[98:101], v196 offset:20480
	ds_read_b128 v[102:105], v197 offset:20480
	ds_read_b128 v[206:209], v196 offset:26624
	ds_read_b128 v[210:213], v197 offset:26624
	v_add_f32_e32 v182, v236, v235
	s_waitcnt lgkmcnt(0)
	v_mfma_f32_32x32x64_f8f6f4 v[114:129], v[98:105], v[138:145], v[66:81]
	v_add_f32_e32 v182, v233, v182
	v_add_f32_e32 v182, v234, v182
	v_add_f32_e32 v182, v231, v182
	v_add_f32_e32 v182, v232, v182
	v_add_f32_e32 v182, v229, v182
	v_add_f32_e32 v182, v230, v182
	v_add_f32_e32 v182, v227, v182
	v_add_f32_e32 v182, v228, v182
	v_add_f32_e32 v182, v225, v182
	v_add_f32_e32 v182, v226, v182
	v_exp_f32_e32 v82, v82
	v_add_f32_e32 v182, v223, v182
	v_exp_f32_e32 v83, v83
	v_add_f32_e32 v182, v224, v182
	v_exp_f32_e32 v84, v84
	v_mfma_f32_32x32x64_f8f6f4 v[98:113], v[206:213], v[138:145], v[66:81]
	ds_read_b128 v[206:209], v198 offset:20480
	ds_read_b128 v[210:213], v199 offset:20480
	ds_read_b128 v[238:241], v198 offset:26624
	ds_read_b128 v[242:245], v199 offset:26624
	s_setprio 1
	v_add_f32_e32 v182, v221, v182
	v_exp_f32_e32 v85, v85
	v_add_f32_e32 v182, v222, v182
	v_exp_f32_e32 v86, v86
	v_add_f32_e32 v182, v82, v182
	v_exp_f32_e32 v87, v87
	v_add_f32_e32 v182, v83, v182
	v_exp_f32_e32 v88, v88
	v_add_f32_e32 v182, v84, v182
	v_exp_f32_e32 v89, v89
	v_add_f32_e32 v182, v85, v182
	v_exp_f32_e32 v90, v90
	v_add_f32_e32 v182, v86, v182
	v_exp_f32_e32 v91, v91
	s_waitcnt lgkmcnt(0)
	v_mfma_f32_32x32x64_f8f6f4 v[114:129], v[206:213], v[146:153], v[114:129]
	v_add_f32_e32 v182, v87, v182
	v_exp_f32_e32 v92, v92
	v_exp_f32_e32 v94, v94
	v_exp_f32_e32 v95, v95
	v_add_f32_e32 v182, v88, v182
	v_exp_f32_e32 v93, v93
	v_add_f32_e32 v182, v89, v182
	v_add_f32_e32 v182, v90, v182
	v_add_f32_e32 v182, v91, v182
	v_exp_f32_e32 v96, v96
	v_exp_f32_e32 v97, v97
	v_add_f32_e32 v182, v92, v182
	v_cvt_pk_fp8_f32 v130, v235, v236
	v_cvt_pk_fp8_f32 v134, v82, v83
	v_cvt_pk_fp8_f32 v131, v231, v232
	v_mfma_f32_32x32x64_f8f6f4 v[98:113], v[238:245], v[146:153], v[98:113]
	ds_read_b128 v[206:209], v200 offset:20480
	ds_read_b128 v[210:213], v201 offset:20480
	ds_read_b128 v[238:241], v200 offset:26624
	ds_read_b128 v[242:245], v201 offset:26624
	v_cvt_pk_fp8_f32 v135, v86, v87
	v_cvt_pk_fp8_f32 v132, v227, v228
	v_cvt_pk_fp8_f32 v136, v90, v91
	v_cvt_pk_fp8_f32 v133, v223, v224
	v_cvt_pk_fp8_f32 v137, v94, v95
	v_add_f32_e32 v182, v93, v182
	v_add_f32_e32 v182, v94, v182
	v_add_f32_e32 v182, v95, v182
	v_add_f32_e32 v182, v96, v182
	v_cvt_pk_fp8_f32 v130, v233, v234 op_sel:[0,0,1]
	v_cvt_pk_fp8_f32 v134, v84, v85 op_sel:[0,0,1]
	v_cvt_pk_fp8_f32 v131, v229, v230 op_sel:[0,0,1]
	v_cvt_pk_fp8_f32 v135, v88, v89 op_sel:[0,0,1]
	v_cvt_pk_fp8_f32 v132, v225, v226 op_sel:[0,0,1]
	s_waitcnt lgkmcnt(0)
	v_mfma_f32_32x32x64_f8f6f4 v[114:129], v[206:213], v[154:161], v[114:129]
	v_cvt_pk_fp8_f32 v136, v92, v93 op_sel:[0,0,1]
	v_cvt_pk_fp8_f32 v133, v221, v222 op_sel:[0,0,1]
	v_cvt_pk_fp8_f32 v137, v96, v97 op_sel:[0,0,1]
	v_add_f32_e32 v206, v97, v182
	v_mov_b32_e32 v207, v206
	s_nop 1
	v_permlane32_swap_b32_e32 v206, v207
	v_mfma_f32_32x32x64_f8f6f4 v[98:113], v[238:245], v[154:161], v[98:113]
	s_cmp_eq_u32 s94, 0
	s_cbranch_scc0 .Lstg_mid0_l0
	s_waitcnt vmcnt(0)
	s_barrier
	s_mov_b32 m0, s87
	s_nop 0
	global_load_lds_dwordx4 v164, s[24:25]
	s_mov_b32 m0, s89
	s_nop 0
	global_load_lds_dwordx4 v170, s[26:27]
	s_add_u32 s24, s24, 0x3000
	s_addc_u32 s25, s25, 0
	s_add_u32 s26, s26, 64
	s_addc_u32 s27, s27, 0
.Lstg_mid0_l0:
	v_add_u32_e32 v194, v204, v203
	v_add_u32_e32 v193, v204, v202
	ds_read_b128 v[86:89], v194
	ds_read_b128 v[82:85], v193
	ds_read_b128 v[90:93], v193 offset:2048
	ds_read_b128 v[94:97], v194 offset:2048
	s_nop 4
	v_max_f32_e32 v182, v114, v115
	s_waitcnt lgkmcnt(0)
	v_mfma_f32_32x32x64_f8f6f4 v[2:17], v[130:137], v[82:89], v[2:17]
	v_max3_f32 v182, v182, v116, v117
	v_max3_f32 v182, v182, v118, v119
	v_max3_f32 v182, v182, v120, v121
	v_max3_f32 v182, v182, v122, v123
	v_max3_f32 v182, v182, v124, v125
	v_max3_f32 v182, v182, v126, v127
	v_max3_f32 v182, v182, v128, v129
	v_max3_f32 v182, v182, v98, v99
	v_mov_b32_e32 v208, 1.0
	v_mfma_f32_32x32x64_f8f6f4 v[50:65], v[130:137], v[90:97], v[50:65]
	ds_read_b128 v[82:85], v193 offset:4096
	ds_read_b128 v[90:93], v193 offset:6144
	ds_read_b128 v[86:89], v194 offset:4096
	ds_read_b128 v[94:97], v194 offset:6144
	s_waitcnt lgkmcnt(0)
	v_mfma_f32_32x32x64_f8f6f4 v[34:49], v[130:137], v[82:89], v[34:49]
	v_max3_f32 v82, v182, v100, v101
	v_max3_f32 v82, v82, v102, v103
	v_max3_f32 v82, v82, v104, v105
	v_max3_f32 v82, v82, v106, v107
	v_max3_f32 v82, v82, v108, v109
	v_max3_f32 v82, v82, v110, v111
	v_max3_f32 v82, v82, v112, v113
	v_mov_b32_e32 v83, v82
	s_nop 1
	v_permlane32_swap_b32_e32 v82, v83
	v_max_f32_e32 v82, v82, v83
	v_cmp_ge_f32_e32 vcc, s85, v82
	s_cmp_eq_u64 vcc, exec
	v_mfma_f32_32x32x64_f8f6f4 v[18:33], v[130:137], v[90:97], v[18:33]
	s_cbranch_scc0 .LBB0_931
	s_setprio 0
	s_branch .LBB0_894

; template <bool FIRST>
; __device__ __forceinline__ void partialSM(f32x16& p0, f32x16& p1, float& m_reg, f32x16& nm16, float& alpha) {
;   float pmax = p0[0];
; #pragma unroll
;   for (int r = 1; r < 16; ++r) pmax = fmaxf(pmax, p0[r]);
; #pragma unroll
;   for (int r = 0; r < 16; ++r) pmax = fmaxf(pmax, p1[r]);
;   { auto rr = __builtin_amdgcn_permlane32_swap(__float_as_uint(pmax), __float_as_uint(pmax), false, false);
;     pmax = fmaxf(__uint_as_float(rr[0]), __uint_as_float(rr[1])); }
;   if (!FIRST && __builtin_expect(__all(pmax <= THR2), 1)) { alpha = 1.f; }
;   else { const float d = FIRST ? pmax : fmaxf(pmax, 0.f);
;     alpha = FIRST ? 1.f : __builtin_amdgcn_exp2f(-d); m_reg += d;
;     const float nm = -m_reg;
; #pragma unroll
;     for (int r = 0; r < 16; ++r) { p0[r] -= d; p1[r] -= d; float t = nm16[r]; asm volatile("v_mov_b32 %0, %1" : "+v"(t) : "v"(nm)); nm16[r] = t; } }
; #pragma unroll
;   for (int r = 0; r < 16; ++r) p0[r] = __builtin_amdgcn_exp2f(p0[r]);
; }
; __device__ __forceinline__ void finishSM(f32x16& p0, f32x16& p1, float alpha, float& l_reg, v8i& pa) {
; #pragma unroll
;   for (int r = 0; r < 16; ++r) p1[r] = __builtin_amdgcn_exp2f(p1[r]);
;   float ps = 0;
; #pragma unroll
;   for (int r = 0; r < 16; ++r) ps += p0[r];
; #pragma unroll
;   for (int r = 0; r < 16; ++r) ps += p1[r];
;   { auto rr = __builtin_amdgcn_permlane32_swap(__float_as_uint(ps), __float_as_uint(ps), false, false);
;     ps = __uint_as_float(rr[0]) + __uint_as_float(rr[1]); }
;   l_reg = l_reg * alpha + ps;
; #pragma unroll
;   for (int q = 0; q < 4; ++q) { int w0 = pa[q], w1 = pa[4 + q];
;     w0 = __builtin_amdgcn_cvt_pk_fp8_f32(p0[4 * q], p0[4 * q + 1], w0, false); w0 = __builtin_amdgcn_cvt_pk_fp8_f32(p0[4 * q + 2], p0[4 * q + 3], w0, true);
;     w1 = __builtin_amdgcn_cvt_pk_fp8_f32(p1[4 * q], p1[4 * q + 1], w1, false); w1 = __builtin_amdgcn_cvt_pk_fp8_f32(p1[4 * q + 2], p1[4 * q + 3], w1, true);
;     pa[q] = w0; pa[4 + q] = w1; }
; }
; __device__ __forceinline__ void qkt(f32x16& p0, f32x16& p1, const char* Ks, const v8i* qr, int r32, int hi, const f32x16& nm16) {
; #pragma unroll
;   for (int s = 0; s < 3; ++s) { const int c0 = 4 * s + 2 * hi;
;     const v8i a0 = __builtin_shufflevector(*reinterpret_cast<const v4i*>(Ks + k8_off(r32, c0)), *reinterpret_cast<const v4i*>(Ks + k8_off(r32, c0 + 1)), 0, 1, 2, 3, 4, 5, 6, 7);
.Lstg_end0_l0:
	v_exp_f32_e32 v182, v114
	v_exp_f32_e32 v183, v115
	v_exp_f32_e32 v184, v116
	v_exp_f32_e32 v185, v117
	v_exp_f32_e32 v226, v118
	v_exp_f32_e32 v227, v119
	v_exp_f32_e32 v228, v120
	v_exp_f32_e32 v229, v121
	v_exp_f32_e32 v230, v122
	v_exp_f32_e32 v231, v123
	v_exp_f32_e32 v232, v124
	v_exp_f32_e32 v233, v125
	v_exp_f32_e32 v234, v126
	v_exp_f32_e32 v235, v127
	v_exp_f32_e32 v236, v128
	v_exp_f32_e32 v237, v129
	ds_read_b128 v[82:85], v196 offset:49152
	ds_read_b128 v[86:89], v197 offset:49152
	ds_read_b128 v[210:213], v196 offset:55296
	ds_read_b128 v[214:217], v197 offset:55296
	v_add_f32_e32 v209, v183, v182
	s_waitcnt lgkmcnt(0)
	v_mfma_f32_32x32x64_f8f6f4 v[114:129], v[82:89], v[138:145], v[66:81]
	v_add_f32_e32 v209, v184, v209
	v_add_f32_e32 v209, v185, v209
	v_add_f32_e32 v209, v226, v209
	v_add_f32_e32 v209, v227, v209
	v_add_f32_e32 v209, v228, v209
	v_add_f32_e32 v209, v229, v209
	v_add_f32_e32 v209, v230, v209
	v_add_f32_e32 v209, v231, v209
	v_add_f32_e32 v209, v232, v209
	v_add_f32_e32 v209, v233, v209
	v_exp_f32_e32 v98, v98
	v_add_f32_e32 v209, v234, v209
	v_exp_f32_e32 v99, v99
	v_add_f32_e32 v209, v235, v209
	v_exp_f32_e32 v100, v100
	v_mfma_f32_32x32x64_f8f6f4 v[82:97], v[210:217], v[138:145], v[66:81]
	ds_read_b128 v[210:213], v198 offset:49152
	ds_read_b128 v[214:217], v199 offset:49152
	ds_read_b128 v[218:221], v198 offset:55296
	ds_read_b128 v[222:225], v199 offset:55296
	s_setprio 1
	v_add_f32_e32 v209, v236, v209
	v_exp_f32_e32 v101, v101
	v_add_f32_e32 v209, v237, v209
	v_exp_f32_e32 v102, v102
	v_add_f32_e32 v209, v98, v209
	v_exp_f32_e32 v103, v103
	v_add_f32_e32 v209, v99, v209
	v_exp_f32_e32 v104, v104
	v_add_f32_e32 v209, v100, v209
	v_exp_f32_e32 v105, v105
	v_add_f32_e32 v209, v101, v209
	v_exp_f32_e32 v106, v106
	v_add_f32_e32 v209, v102, v209
	v_exp_f32_e32 v107, v107
	s_waitcnt lgkmcnt(0)
	v_mfma_f32_32x32x64_f8f6f4 v[114:129], v[210:217], v[146:153], v[114:129]
	v_add_f32_e32 v209, v103, v209
	v_exp_f32_e32 v108, v108
	v_exp_f32_e32 v110, v110
	v_exp_f32_e32 v111, v111
	v_add_f32_e32 v209, v104, v209
	v_exp_f32_e32 v109, v109
	v_add_f32_e32 v209, v105, v209
	v_add_f32_e32 v209, v106, v209
	v_add_f32_e32 v209, v107, v209
	v_exp_f32_e32 v112, v112
	v_exp_f32_e32 v113, v113
	v_add_f32_e32 v209, v108, v209
	v_cvt_pk_fp8_f32 v130, v182, v183
	v_cvt_pk_fp8_f32 v134, v98, v99
	v_cvt_pk_fp8_f32 v131, v226, v227
	v_mfma_f32_32x32x64_f8f6f4 v[82:97], v[218:225], v[146:153], v[82:97]
	ds_read_b128 v[210:213], v200 offset:49152
	ds_read_b128 v[214:217], v201 offset:49152
	ds_read_b128 v[218:221], v200 offset:55296
	ds_read_b128 v[222:225], v201 offset:55296
	v_cvt_pk_fp8_f32 v135, v102, v103
	v_cvt_pk_fp8_f32 v132, v230, v231
	v_cvt_pk_fp8_f32 v136, v106, v107
	v_cvt_pk_fp8_f32 v133, v234, v235
	v_cvt_pk_fp8_f32 v137, v110, v111
	v_add_f32_e32 v209, v109, v209
	v_add_f32_e32 v209, v110, v209
	v_add_f32_e32 v209, v111, v209
	v_add_f32_e32 v209, v112, v209
	v_cvt_pk_fp8_f32 v130, v184, v185 op_sel:[0,0,1]
	v_cvt_pk_fp8_f32 v134, v100, v101 op_sel:[0,0,1]
	v_cvt_pk_fp8_f32 v131, v228, v229 op_sel:[0,0,1]
	v_cvt_pk_fp8_f32 v135, v104, v105 op_sel:[0,0,1]
	v_cvt_pk_fp8_f32 v132, v232, v233 op_sel:[0,0,1]
	s_waitcnt lgkmcnt(0)
	v_mfma_f32_32x32x64_f8f6f4 v[114:129], v[210:217], v[154:161], v[114:129]
	v_cvt_pk_fp8_f32 v136, v108, v109 op_sel:[0,0,1]
	v_cvt_pk_fp8_f32 v133, v236, v237 op_sel:[0,0,1]
	v_cvt_pk_fp8_f32 v137, v112, v113 op_sel:[0,0,1]
	v_add_f32_e32 v209, v113, v209
	v_mov_b32_e32 v210, v209
	s_nop 1
	v_permlane32_swap_b32_e32 v209, v210
	v_mfma_f32_32x32x64_f8f6f4 v[82:97], v[218:225], v[154:161], v[82:97]
	s_cmp_eq_u32 s94, 0
	s_cbranch_scc0 .Lstg_mid1_l0
	s_waitcnt vmcnt(0)
	s_barrier
	s_mov_b32 m0, s92
	s_nop 0
	global_load_lds_dwordx4 v164, s[24:25]
	s_mov_b32 m0, s86
	s_nop 0
	global_load_lds_dwordx4 v170, s[26:27]
	s_add_u32 s24, s24, 0x3000
	s_addc_u32 s25, s25, 0
	s_add_u32 s26, s26, 64
	s_addc_u32 s27, s27, 0
.Lstg_mid1_l0:
	ds_read_b128 v[102:105], v194 offset:32768
	ds_read_b128 v[98:101], v193 offset:32768
	ds_read_b128 v[106:109], v193 offset:34816
	ds_read_b128 v[110:113], v194 offset:34816
	s_nop 6
	v_max_f32_e32 v182, v114, v115
	s_waitcnt lgkmcnt(0)
	v_mfma_f32_32x32x64_f8f6f4 v[2:17], v[130:137], v[98:105], v[2:17]
	v_max3_f32 v182, v182, v116, v117
	v_max3_f32 v182, v182, v118, v119
	v_max3_f32 v182, v182, v120, v121
	v_max3_f32 v182, v182, v122, v123
	v_max3_f32 v182, v182, v124, v125
	v_max3_f32 v182, v182, v126, v127
	v_max3_f32 v182, v182, v128, v129
	v_max3_f32 v182, v182, v82, v83
	v_mov_b32_e32 v211, 1.0
	v_mfma_f32_32x32x64_f8f6f4 v[50:65], v[130:137], v[106:113], v[50:65]
	ds_read_b128 v[98:101], v193 offset:36864
	ds_read_b128 v[106:109], v193 offset:38912
	ds_read_b128 v[102:105], v194 offset:36864
	ds_read_b128 v[110:113], v194 offset:38912
	s_waitcnt lgkmcnt(0)
	v_mfma_f32_32x32x64_f8f6f4 v[34:49], v[130:137], v[98:105], v[34:49]
	v_max3_f32 v98, v182, v84, v85
	v_max3_f32 v98, v98, v86, v87
	v_max3_f32 v98, v98, v88, v89
	v_max3_f32 v98, v98, v90, v91
	v_max3_f32 v98, v98, v92, v93
	v_max3_f32 v98, v98, v94, v95
	v_max3_f32 v98, v98, v96, v97
	v_mov_b32_e32 v99, v98
	s_nop 1
	v_permlane32_swap_b32_e32 v98, v99
	v_max_f32_e32 v98, v98, v99
	v_cmp_ge_f32_e32 vcc, s85, v98
	s_cmp_eq_u64 vcc, exec
	v_mfma_f32_32x32x64_f8f6f4 v[18:33], v[130:137], v[106:113], v[18:33]
	s_cbranch_scc0 .LBB0_932
	s_setprio 0
	s_branch .LBB0_901

; template <bool FIRST>
; __device__ __forceinline__ void partialSM(f32x16& p0, f32x16& p1, float& m_reg, f32x16& nm16, float& alpha) {
;   float pmax = p0[0];
; #pragma unroll
;   for (int r = 1; r < 16; ++r) pmax = fmaxf(pmax, p0[r]);
; #pragma unroll
;   for (int r = 0; r < 16; ++r) pmax = fmaxf(pmax, p1[r]);
;   { auto rr = __builtin_amdgcn_permlane32_swap(__float_as_uint(pmax), __float_as_uint(pmax), false, false);
;     pmax = fmaxf(__uint_as_float(rr[0]), __uint_as_float(rr[1])); }
;   if (!FIRST && __builtin_expect(__all(pmax <= THR2), 1)) { alpha = 1.f; }
;   else { const float d = FIRST ? pmax : fmaxf(pmax, 0.f);
;     alpha = FIRST ? 1.f : __builtin_amdgcn_exp2f(-d); m_reg += d;
;     const float nm = -m_reg;
; #pragma unroll
;     for (int r = 0; r < 16; ++r) { p0[r] -= d; p1[r] -= d; float t = nm16[r]; asm volatile("v_mov_b32 %0, %1" : "+v"(t) : "v"(nm)); nm16[r] = t; } }
; #pragma unroll
;   for (int r = 0; r < 16; ++r) p0[r] = __builtin_amdgcn_exp2f(p0[r]);
; }
; __device__ __forceinline__ void finishSM(f32x16& p0, f32x16& p1, float alpha, float& l_reg, v8i& pa) {
; #pragma unroll
;   for (int r = 0; r < 16; ++r) p1[r] = __builtin_amdgcn_exp2f(p1[r]);
;   float ps = 0;
; #pragma unroll
;   for (int r = 0; r < 16; ++r) ps += p0[r];
; #pragma unroll
;   for (int r = 0; r < 16; ++r) ps += p1[r];
;   { auto rr = __builtin_amdgcn_permlane32_swap(__float_as_uint(ps), __float_as_uint(ps), false, false);
;     ps = __uint_as_float(rr[0]) + __uint_as_float(rr[1]); }
;   l_reg = l_reg * alpha + ps;
; #pragma unroll
;   for (int q = 0; q < 4; ++q) { int w0 = pa[q], w1 = pa[4 + q];
;     w0 = __builtin_amdgcn_cvt_pk_fp8_f32(p0[4 * q], p0[4 * q + 1], w0, false); w0 = __builtin_amdgcn_cvt_pk_fp8_f32(p0[4 * q + 2], p0[4 * q + 3], w0, true);
;     w1 = __builtin_amdgcn_cvt_pk_fp8_f32(p1[4 * q], p1[4 * q + 1], w1, false); w1 = __builtin_amdgcn_cvt_pk_fp8_f32(p1[4 * q + 2], p1[4 * q + 3], w1, true);
;     pa[q] = w0; pa[4 + q] = w1; }
; }
; __device__ __forceinline__ void qkt(f32x16& p0, f32x16& p1, const char* Ks, const v8i* qr, int r32, int hi, const f32x16& nm16) {
; #pragma unroll
;   for (int s = 0; s < 3; ++s) { const int c0 = 4 * s + 2 * hi;
;     const v8i a0 = __builtin_shufflevector(*reinterpret_cast<const v4i*>(Ks + k8_off(r32, c0)), *reinterpret_cast<const v4i*>(Ks + k8_off(r32, c0 + 1)), 0, 1, 2, 3, 4, 5, 6, 7);
.Lstg_end1_l0:
	v_exp_f32_e32 v182, v114
	v_exp_f32_e32 v183, v115
	v_exp_f32_e32 v184, v116
	v_exp_f32_e32 v185, v117
	v_exp_f32_e32 v228, v118
	v_exp_f32_e32 v229, v119
	v_exp_f32_e32 v230, v120
	v_exp_f32_e32 v231, v121
	v_exp_f32_e32 v232, v122
	v_exp_f32_e32 v233, v123
	v_exp_f32_e32 v234, v124
	v_exp_f32_e32 v235, v125
	v_exp_f32_e32 v236, v126
	v_exp_f32_e32 v237, v127
	v_exp_f32_e32 v238, v128
	v_exp_f32_e32 v239, v129
	ds_read_b128 v[98:101], v196 offset:8192
	ds_read_b128 v[102:105], v197 offset:8192
	ds_read_b128 v[212:215], v196 offset:14336
	ds_read_b128 v[216:219], v197 offset:14336
	v_exp_f32_e32 v82, v82
	v_exp_f32_e32 v83, v83
	s_waitcnt lgkmcnt(0)
	v_mfma_f32_32x32x64_f8f6f4 v[114:129], v[98:105], v[138:145], v[66:81]
	v_exp_f32_e32 v84, v84
	v_exp_f32_e32 v85, v85
	v_exp_f32_e32 v86, v86
	v_exp_f32_e32 v87, v87
	v_exp_f32_e32 v88, v88
	v_exp_f32_e32 v89, v89
	v_exp_f32_e32 v90, v90
	v_exp_f32_e32 v91, v91
	v_exp_f32_e32 v92, v92
	v_exp_f32_e32 v94, v94
	v_exp_f32_e32 v95, v95
	v_exp_f32_e32 v93, v93
	v_exp_f32_e32 v96, v96
	v_exp_f32_e32 v97, v97
	v_cvt_pk_fp8_f32 v130, v182, v183
	v_mfma_f32_32x32x64_f8f6f4 v[98:113], v[212:219], v[138:145], v[66:81]
	ds_read_b128 v[212:215], v198 offset:8192
	ds_read_b128 v[216:219], v199 offset:8192
	ds_read_b128 v[220:223], v198 offset:14336
	ds_read_b128 v[224:227], v199 offset:14336
	s_setprio 1
	v_cvt_pk_fp8_f32 v134, v82, v83
	v_cvt_pk_fp8_f32 v131, v228, v229
	v_cvt_pk_fp8_f32 v135, v86, v87
	v_cvt_pk_fp8_f32 v132, v232, v233
	v_cvt_pk_fp8_f32 v136, v90, v91
	v_cvt_pk_fp8_f32 v133, v236, v237
	v_cvt_pk_fp8_f32 v137, v94, v95
	v_cvt_pk_fp8_f32 v130, v184, v185 op_sel:[0,0,1]
	v_cvt_pk_fp8_f32 v134, v84, v85 op_sel:[0,0,1]
	v_cvt_pk_fp8_f32 v131, v230, v231 op_sel:[0,0,1]
	v_cvt_pk_fp8_f32 v135, v88, v89 op_sel:[0,0,1]
	v_cvt_pk_fp8_f32 v132, v234, v235 op_sel:[0,0,1]
	v_cvt_pk_fp8_f32 v136, v92, v93 op_sel:[0,0,1]
	v_cvt_pk_fp8_f32 v133, v238, v239 op_sel:[0,0,1]
	s_waitcnt lgkmcnt(0)
	v_mfma_f32_32x32x64_f8f6f4 v[114:129], v[212:219], v[146:153], v[114:129]
	v_cvt_pk_fp8_f32 v137, v96, v97 op_sel:[0,0,1]
	v_mfma_f32_32x32x64_f8f6f4 v[98:113], v[220:227], v[146:153], v[98:113]
	ds_read_b128 v[212:215], v200 offset:8192
	ds_read_b128 v[216:219], v201 offset:8192
	ds_read_b128 v[220:223], v200 offset:14336
	ds_read_b128 v[224:227], v201 offset:14336
	s_waitcnt lgkmcnt(0)
	v_mfma_f32_32x32x64_f8f6f4 v[114:129], v[212:219], v[154:161], v[114:129]
	v_add_f32_e32 v212, v183, v182
	v_add_f32_e32 v212, v184, v212
	v_add_f32_e32 v212, v185, v212
	v_add_f32_e32 v212, v228, v212
	v_add_f32_e32 v212, v229, v212
	v_add_f32_e32 v212, v230, v212
	v_add_f32_e32 v212, v231, v212
	v_add_f32_e32 v212, v232, v212
	v_add_f32_e32 v212, v233, v212
	v_add_f32_e32 v212, v234, v212
	v_add_f32_e32 v212, v235, v212
	v_add_f32_e32 v212, v236, v212
	v_add_f32_e32 v212, v237, v212
	v_add_f32_e32 v212, v238, v212
	v_add_f32_e32 v212, v239, v212
	v_add_f32_e32 v212, v82, v212
	v_add_f32_e32 v212, v83, v212
	v_mfma_f32_32x32x64_f8f6f4 v[98:113], v[220:227], v[154:161], v[98:113]
	v_add_f32_e32 v212, v84, v212
	v_add_f32_e32 v212, v85, v212
	v_add_f32_e32 v212, v86, v212
	v_add_f32_e32 v212, v87, v212
	v_add_f32_e32 v212, v88, v212
	v_add_f32_e32 v212, v89, v212
	v_add_f32_e32 v212, v90, v212
	v_add_f32_e32 v212, v91, v212
	v_add_f32_e32 v212, v92, v212
	v_add_f32_e32 v212, v93, v212
	v_add_f32_e32 v212, v94, v212
	v_add_f32_e32 v212, v95, v212
	v_add_f32_e32 v212, v96, v212
	v_add_f32_e32 v212, v97, v212
	v_mov_b32_e32 v213, v212
	s_nop 1
	v_permlane32_swap_b32_e32 v212, v213
	s_cmp_eq_u32 s94, 0
	s_cbranch_scc0 .Lstg_mid2_l0
	s_waitcnt vmcnt(0)
	s_barrier
	s_mov_b32 m0, s90
	s_nop 0
	global_load_lds_dwordx4 v164, s[24:25]
	s_mov_b32 m0, s88
	s_nop 0
	global_load_lds_dwordx4 v170, s[26:27]
	s_add_u32 s24, s24, 0x3000
	s_addc_u32 s25, s25, 0
	s_add_u32 s26, s26, 64
	s_addc_u32 s27, s27, 0
.Lstg_mid2_l0:
	ds_read_b128 v[86:89], v194 offset:40960
	ds_read_b128 v[82:85], v193 offset:40960
	ds_read_b128 v[90:93], v193 offset:43008
	ds_read_b128 v[94:97], v194 offset:43008
	v_max_f32_e32 v182, v114, v115
	s_waitcnt lgkmcnt(0)
	v_mfma_f32_32x32x64_f8f6f4 v[2:17], v[130:137], v[82:89], v[2:17]
	v_max3_f32 v182, v182, v116, v117
	v_max3_f32 v182, v182, v118, v119
	v_max3_f32 v182, v182, v120, v121
	v_max3_f32 v182, v182, v122, v123
	v_max3_f32 v182, v182, v124, v125
	v_max3_f32 v182, v182, v126, v127
	v_max3_f32 v182, v182, v128, v129
	v_max3_f32 v182, v182, v98, v99
	v_mov_b32_e32 v214, 1.0
	v_mfma_f32_32x32x64_f8f6f4 v[50:65], v[130:137], v[90:97], v[50:65]
	ds_read_b128 v[82:85], v193 offset:45056
	ds_read_b128 v[90:93], v193 offset:47104
	ds_read_b128 v[86:89], v194 offset:45056
	ds_read_b128 v[94:97], v194 offset:47104
	s_waitcnt lgkmcnt(0)
	v_mfma_f32_32x32x64_f8f6f4 v[34:49], v[130:137], v[82:89], v[34:49]
	v_max3_f32 v82, v182, v100, v101
	v_max3_f32 v82, v82, v102, v103
	v_max3_f32 v82, v82, v104, v105
	v_max3_f32 v82, v82, v106, v107
	v_max3_f32 v82, v82, v108, v109
	v_max3_f32 v82, v82, v110, v111
	v_max3_f32 v82, v82, v112, v113
	v_mov_b32_e32 v83, v82
	s_nop 1
	v_permlane32_swap_b32_e32 v82, v83
	v_max_f32_e32 v82, v82, v83
	v_cmp_ge_f32_e32 vcc, s85, v82
	s_cmp_eq_u64 vcc, exec
	v_mfma_f32_32x32x64_f8f6f4 v[18:33], v[130:137], v[90:97], v[18:33]
	s_cbranch_scc0 .LBB0_933
	s_setprio 0
	s_branch .LBB0_908

; template <bool FIRST>
; __device__ __forceinline__ void partialSM(f32x16& p0, f32x16& p1, float& m_reg, f32x16& nm16, float& alpha) {
;   float pmax = p0[0];
; #pragma unroll
;   for (int r = 1; r < 16; ++r) pmax = fmaxf(pmax, p0[r]);
; #pragma unroll
;   for (int r = 0; r < 16; ++r) pmax = fmaxf(pmax, p1[r]);
;   { auto rr = __builtin_amdgcn_permlane32_swap(__float_as_uint(pmax), __float_as_uint(pmax), false, false);
;     pmax = fmaxf(__uint_as_float(rr[0]), __uint_as_float(rr[1])); }
;   if (!FIRST && __builtin_expect(__all(pmax <= THR2), 1)) { alpha = 1.f; }
;   else { const float d = FIRST ? pmax : fmaxf(pmax, 0.f);
;     alpha = FIRST ? 1.f : __builtin_amdgcn_exp2f(-d); m_reg += d;
;     const float nm = -m_reg;
; #pragma unroll
;     for (int r = 0; r < 16; ++r) { p0[r] -= d; p1[r] -= d; float t = nm16[r]; asm volatile("v_mov_b32 %0, %1" : "+v"(t) : "v"(nm)); nm16[r] = t; } }
; #pragma unroll
;   for (int r = 0; r < 16; ++r) p0[r] = __builtin_amdgcn_exp2f(p0[r]);
; }
; __device__ __forceinline__ void finishSM(f32x16& p0, f32x16& p1, float alpha, float& l_reg, v8i& pa) {
; #pragma unroll
;   for (int r = 0; r < 16; ++r) p1[r] = __builtin_amdgcn_exp2f(p1[r]);
;   float ps = 0;
; #pragma unroll
;   for (int r = 0; r < 16; ++r) ps += p0[r];
; #pragma unroll
;   for (int r = 0; r < 16; ++r) ps += p1[r];
;   { auto rr = __builtin_amdgcn_permlane32_swap(__float_as_uint(ps), __float_as_uint(ps), false, false);
;     ps = __uint_as_float(rr[0]) + __uint_as_float(rr[1]); }
;   l_reg = l_reg * alpha + ps;
; #pragma unroll
;   for (int q = 0; q < 4; ++q) { int w0 = pa[q], w1 = pa[4 + q];
;     w0 = __builtin_amdgcn_cvt_pk_fp8_f32(p0[4 * q], p0[4 * q + 1], w0, false); w0 = __builtin_amdgcn_cvt_pk_fp8_f32(p0[4 * q + 2], p0[4 * q + 3], w0, true);
;     w1 = __builtin_amdgcn_cvt_pk_fp8_f32(p1[4 * q], p1[4 * q + 1], w1, false); w1 = __builtin_amdgcn_cvt_pk_fp8_f32(p1[4 * q + 2], p1[4 * q + 3], w1, true);
;     pa[q] = w0; pa[4 + q] = w1; }
; }
; __device__ __forceinline__ void qkt(f32x16& p0, f32x16& p1, const char* Ks, const v8i* qr, int r32, int hi, const f32x16& nm16) {
; #pragma unroll
;   for (int s = 0; s < 3; ++s) { const int c0 = 4 * s + 2 * hi;
;     const v8i a0 = __builtin_shufflevector(*reinterpret_cast<const v4i*>(Ks + k8_off(r32, c0)), *reinterpret_cast<const v4i*>(Ks + k8_off(r32, c0 + 1)), 0, 1, 2, 3, 4, 5, 6, 7);
.Lstg_end2_l0:
	v_exp_f32_e32 v182, v114
	v_exp_f32_e32 v183, v115
	v_exp_f32_e32 v184, v116
	v_exp_f32_e32 v185, v117
	v_exp_f32_e32 v232, v118
	v_exp_f32_e32 v233, v119
	v_exp_f32_e32 v234, v120
	v_exp_f32_e32 v235, v121
	v_exp_f32_e32 v236, v122
	v_exp_f32_e32 v237, v123
	v_exp_f32_e32 v238, v124
	v_exp_f32_e32 v239, v125
	v_exp_f32_e32 v240, v126
	v_exp_f32_e32 v241, v127
	v_exp_f32_e32 v242, v128
	v_exp_f32_e32 v243, v129
	ds_read_b128 v[82:85], v196 offset:20480
	ds_read_b128 v[86:89], v197 offset:20480
	ds_read_b128 v[216:219], v196 offset:26624
	ds_read_b128 v[220:223], v197 offset:26624
	v_add_f32_e32 v215, v183, v182
	s_waitcnt lgkmcnt(0)
	v_mfma_f32_32x32x64_f8f6f4 v[114:129], v[82:89], v[138:145], v[66:81]
	v_add_f32_e32 v215, v184, v215
	v_add_f32_e32 v215, v185, v215
	v_add_f32_e32 v215, v232, v215
	v_add_f32_e32 v215, v233, v215
	v_add_f32_e32 v215, v234, v215
	v_add_f32_e32 v215, v235, v215
	v_add_f32_e32 v215, v236, v215
	v_add_f32_e32 v215, v237, v215
	v_add_f32_e32 v215, v238, v215
	v_add_f32_e32 v215, v239, v215
	v_exp_f32_e32 v98, v98
	v_add_f32_e32 v215, v240, v215
	v_exp_f32_e32 v99, v99
	v_add_f32_e32 v215, v241, v215
	v_exp_f32_e32 v100, v100
	v_mfma_f32_32x32x64_f8f6f4 v[82:97], v[216:223], v[138:145], v[66:81]
	ds_read_b128 v[216:219], v198 offset:20480
	ds_read_b128 v[220:223], v199 offset:20480
	ds_read_b128 v[224:227], v198 offset:26624
	ds_read_b128 v[228:231], v199 offset:26624
	s_setprio 1
	v_add_f32_e32 v215, v242, v215
	v_exp_f32_e32 v101, v101
	v_add_f32_e32 v215, v243, v215
	v_exp_f32_e32 v102, v102
	v_add_f32_e32 v215, v98, v215
	v_exp_f32_e32 v103, v103
	v_add_f32_e32 v215, v99, v215
	v_exp_f32_e32 v104, v104
	v_add_f32_e32 v215, v100, v215
	v_exp_f32_e32 v105, v105
	v_add_f32_e32 v215, v101, v215
	v_exp_f32_e32 v106, v106
	v_add_f32_e32 v215, v102, v215
	v_exp_f32_e32 v107, v107
	s_waitcnt lgkmcnt(0)
	v_mfma_f32_32x32x64_f8f6f4 v[114:129], v[216:223], v[146:153], v[114:129]
	v_add_f32_e32 v215, v103, v215
	v_exp_f32_e32 v108, v108
	v_exp_f32_e32 v110, v110
	v_exp_f32_e32 v111, v111
	v_add_f32_e32 v215, v104, v215
	v_exp_f32_e32 v109, v109
	v_add_f32_e32 v215, v105, v215
	v_add_f32_e32 v215, v106, v215
	v_add_f32_e32 v215, v107, v215
	v_exp_f32_e32 v112, v112
	v_exp_f32_e32 v113, v113
	v_add_f32_e32 v215, v108, v215
	v_cvt_pk_fp8_f32 v130, v182, v183
	v_cvt_pk_fp8_f32 v134, v98, v99
	v_cvt_pk_fp8_f32 v131, v232, v233
	v_mfma_f32_32x32x64_f8f6f4 v[82:97], v[224:231], v[146:153], v[82:97]
	ds_read_b128 v[216:219], v200 offset:20480
	ds_read_b128 v[220:223], v201 offset:20480
	ds_read_b128 v[224:227], v200 offset:26624
	ds_read_b128 v[228:231], v201 offset:26624
	v_cvt_pk_fp8_f32 v135, v102, v103
	v_cvt_pk_fp8_f32 v132, v236, v237
	v_cvt_pk_fp8_f32 v136, v106, v107
	v_cvt_pk_fp8_f32 v133, v240, v241
	v_cvt_pk_fp8_f32 v137, v110, v111
	v_add_f32_e32 v215, v109, v215
	v_add_f32_e32 v215, v110, v215
	v_add_f32_e32 v215, v111, v215
	v_add_f32_e32 v215, v112, v215
	v_cvt_pk_fp8_f32 v130, v184, v185 op_sel:[0,0,1]
	v_cvt_pk_fp8_f32 v134, v100, v101 op_sel:[0,0,1]
	v_cvt_pk_fp8_f32 v131, v234, v235 op_sel:[0,0,1]
	v_cvt_pk_fp8_f32 v135, v104, v105 op_sel:[0,0,1]
	v_cvt_pk_fp8_f32 v132, v238, v239 op_sel:[0,0,1]
	s_waitcnt lgkmcnt(0)
	v_mfma_f32_32x32x64_f8f6f4 v[114:129], v[216:223], v[154:161], v[114:129]
	v_cvt_pk_fp8_f32 v136, v108, v109 op_sel:[0,0,1]
	v_cvt_pk_fp8_f32 v133, v242, v243 op_sel:[0,0,1]
	v_cvt_pk_fp8_f32 v137, v112, v113 op_sel:[0,0,1]
	v_add_f32_e32 v215, v113, v215
	v_mov_b32_e32 v216, v215
	s_nop 1
	v_permlane32_swap_b32_e32 v215, v216
	v_mfma_f32_32x32x64_f8f6f4 v[82:97], v[224:231], v[154:161], v[82:97]
	s_cmp_eq_u32 s94, 0
	s_cbranch_scc0 .Lstg_mid3_l0
	s_waitcnt vmcnt(0)
	s_barrier
	s_mov_b32 m0, s87
	s_nop 0
	global_load_lds_dwordx4 v164, s[24:25]
	s_mov_b32 m0, s89
	s_nop 0
	global_load_lds_dwordx4 v170, s[26:27]
	s_add_u32 s24, s24, 0x3000
	s_addc_u32 s25, s25, 0
	s_add_u32 s26, s26, 64
	s_addc_u32 s27, s27, 0
.Lstg_mid3_l0:
	ds_read_b128 v[102:105], v194
	ds_read_b128 v[98:101], v193
	ds_read_b128 v[106:109], v193 offset:2048
	ds_read_b128 v[110:113], v194 offset:2048
	s_nop 6
	v_max_f32_e32 v182, v114, v115
	s_waitcnt lgkmcnt(0)
	v_mfma_f32_32x32x64_f8f6f4 v[2:17], v[130:137], v[98:105], v[2:17]
	v_max3_f32 v182, v182, v116, v117
	v_max3_f32 v182, v182, v118, v119
	v_max3_f32 v182, v182, v120, v121
	v_max3_f32 v182, v182, v122, v123
	v_max3_f32 v182, v182, v124, v125
	v_max3_f32 v182, v182, v126, v127
	v_max3_f32 v182, v182, v128, v129
	v_max3_f32 v182, v182, v82, v83
	v_mov_b32_e32 v217, 1.0
	v_mfma_f32_32x32x64_f8f6f4 v[50:65], v[130:137], v[106:113], v[50:65]
	ds_read_b128 v[98:101], v193 offset:4096
	ds_read_b128 v[106:109], v193 offset:6144
	ds_read_b128 v[102:105], v194 offset:4096
	ds_read_b128 v[110:113], v194 offset:6144
	s_waitcnt lgkmcnt(0)
	v_mfma_f32_32x32x64_f8f6f4 v[34:49], v[130:137], v[98:105], v[34:49]
	v_max3_f32 v98, v182, v84, v85
	v_max3_f32 v98, v98, v86, v87
	v_max3_f32 v98, v98, v88, v89
	v_max3_f32 v98, v98, v90, v91
	v_max3_f32 v98, v98, v92, v93
	v_max3_f32 v98, v98, v94, v95
	v_max3_f32 v98, v98, v96, v97
	v_mov_b32_e32 v99, v98
	s_nop 1
	v_permlane32_swap_b32_e32 v98, v99
	v_max_f32_e32 v98, v98, v99
	v_cmp_ge_f32_e32 vcc, s85, v98
	s_cmp_eq_u64 vcc, exec
	v_mfma_f32_32x32x64_f8f6f4 v[18:33], v[130:137], v[106:113], v[18:33]
	s_cbranch_scc0 .LBB0_934
	s_setprio 0
	s_branch .LBB0_915

; template <bool FIRST>
; __device__ __forceinline__ void partialSM(f32x16& p0, f32x16& p1, float& m_reg, f32x16& nm16, float& alpha) {
;   float pmax = p0[0];
; #pragma unroll
;   for (int r = 1; r < 16; ++r) pmax = fmaxf(pmax, p0[r]);
; #pragma unroll
;   for (int r = 0; r < 16; ++r) pmax = fmaxf(pmax, p1[r]);
;   { auto rr = __builtin_amdgcn_permlane32_swap(__float_as_uint(pmax), __float_as_uint(pmax), false, false);
;     pmax = fmaxf(__uint_as_float(rr[0]), __uint_as_float(rr[1])); }
;   if (!FIRST && __builtin_expect(__all(pmax <= THR2), 1)) { alpha = 1.f; }
;   else { const float d = FIRST ? pmax : fmaxf(pmax, 0.f);
;     alpha = FIRST ? 1.f : __builtin_amdgcn_exp2f(-d); m_reg += d;
;     const float nm = -m_reg;
; #pragma unroll
;     for (int r = 0; r < 16; ++r) { p0[r] -= d; p1[r] -= d; float t = nm16[r]; asm volatile("v_mov_b32 %0, %1" : "+v"(t) : "v"(nm)); nm16[r] = t; } }
; #pragma unroll
;   for (int r = 0; r < 16; ++r) p0[r] = __builtin_amdgcn_exp2f(p0[r]);
; }
; __device__ __forceinline__ void finishSM(f32x16& p0, f32x16& p1, float alpha, float& l_reg, v8i& pa) {
; #pragma unroll
;   for (int r = 0; r < 16; ++r) p1[r] = __builtin_amdgcn_exp2f(p1[r]);
;   float ps = 0;
; #pragma unroll
;   for (int r = 0; r < 16; ++r) ps += p0[r];
; #pragma unroll
;   for (int r = 0; r < 16; ++r) ps += p1[r];
;   { auto rr = __builtin_amdgcn_permlane32_swap(__float_as_uint(ps), __float_as_uint(ps), false, false);
;     ps = __uint_as_float(rr[0]) + __uint_as_float(rr[1]); }
;   l_reg = l_reg * alpha + ps;
; #pragma unroll
;   for (int q = 0; q < 4; ++q) { int w0 = pa[q], w1 = pa[4 + q];
;     w0 = __builtin_amdgcn_cvt_pk_fp8_f32(p0[4 * q], p0[4 * q + 1], w0, false); w0 = __builtin_amdgcn_cvt_pk_fp8_f32(p0[4 * q + 2], p0[4 * q + 3], w0, true);
;     w1 = __builtin_amdgcn_cvt_pk_fp8_f32(p1[4 * q], p1[4 * q + 1], w1, false); w1 = __builtin_amdgcn_cvt_pk_fp8_f32(p1[4 * q + 2], p1[4 * q + 3], w1, true);
;     pa[q] = w0; pa[4 + q] = w1; }
; }
; __device__ __forceinline__ void qkt(f32x16& p0, f32x16& p1, const char* Ks, const v8i* qr, int r32, int hi, const f32x16& nm16) {
; #pragma unroll
;   for (int s = 0; s < 3; ++s) { const int c0 = 4 * s + 2 * hi;
;     const v8i a0 = __builtin_shufflevector(*reinterpret_cast<const v4i*>(Ks + k8_off(r32, c0)), *reinterpret_cast<const v4i*>(Ks + k8_off(r32, c0 + 1)), 0, 1, 2, 3, 4, 5, 6, 7);
.Lstg_end3_l0:
	v_exp_f32_e32 v182, v114
	v_exp_f32_e32 v183, v115
	v_exp_f32_e32 v184, v116
	v_exp_f32_e32 v185, v117
	v_exp_f32_e32 v234, v118
	v_exp_f32_e32 v235, v119
	v_exp_f32_e32 v236, v120
	v_exp_f32_e32 v237, v121
	v_exp_f32_e32 v238, v122
	v_exp_f32_e32 v239, v123
	v_exp_f32_e32 v240, v124
	v_exp_f32_e32 v241, v125
	v_exp_f32_e32 v242, v126
	v_exp_f32_e32 v243, v127
	v_exp_f32_e32 v244, v128
	v_exp_f32_e32 v245, v129
	ds_read_b128 v[98:101], v196 offset:49152
	ds_read_b128 v[102:105], v197 offset:49152
	ds_read_b128 v[218:221], v196 offset:55296
	ds_read_b128 v[222:225], v197 offset:55296
	v_exp_f32_e32 v82, v82
	v_exp_f32_e32 v83, v83
	s_waitcnt lgkmcnt(0)
	v_mfma_f32_32x32x64_f8f6f4 v[114:129], v[98:105], v[138:145], v[66:81]
	v_exp_f32_e32 v84, v84
	v_exp_f32_e32 v85, v85
	v_exp_f32_e32 v86, v86
	v_exp_f32_e32 v87, v87
	v_exp_f32_e32 v88, v88
	v_exp_f32_e32 v89, v89
	v_exp_f32_e32 v90, v90
	v_exp_f32_e32 v91, v91
	v_exp_f32_e32 v92, v92
	v_exp_f32_e32 v94, v94
	v_exp_f32_e32 v95, v95
	v_exp_f32_e32 v93, v93
	v_exp_f32_e32 v96, v96
	v_exp_f32_e32 v97, v97
	v_cvt_pk_fp8_f32 v130, v182, v183
	v_mfma_f32_32x32x64_f8f6f4 v[98:113], v[218:225], v[138:145], v[66:81]
	ds_read_b128 v[218:221], v198 offset:49152
	ds_read_b128 v[222:225], v199 offset:49152
	ds_read_b128 v[226:229], v198 offset:55296
	ds_read_b128 v[230:233], v199 offset:55296
	s_setprio 1
	v_cvt_pk_fp8_f32 v134, v82, v83
	v_cvt_pk_fp8_f32 v131, v234, v235
	v_cvt_pk_fp8_f32 v135, v86, v87
	v_cvt_pk_fp8_f32 v132, v238, v239
	v_cvt_pk_fp8_f32 v136, v90, v91
	v_cvt_pk_fp8_f32 v133, v242, v243
	v_cvt_pk_fp8_f32 v137, v94, v95
	v_cvt_pk_fp8_f32 v130, v184, v185 op_sel:[0,0,1]
	v_cvt_pk_fp8_f32 v134, v84, v85 op_sel:[0,0,1]
	v_cvt_pk_fp8_f32 v131, v236, v237 op_sel:[0,0,1]
	v_cvt_pk_fp8_f32 v135, v88, v89 op_sel:[0,0,1]
	v_cvt_pk_fp8_f32 v132, v240, v241 op_sel:[0,0,1]
	v_cvt_pk_fp8_f32 v136, v92, v93 op_sel:[0,0,1]
	v_cvt_pk_fp8_f32 v133, v244, v245 op_sel:[0,0,1]
	s_waitcnt lgkmcnt(0)
	v_mfma_f32_32x32x64_f8f6f4 v[114:129], v[218:225], v[146:153], v[114:129]
	v_cvt_pk_fp8_f32 v137, v96, v97 op_sel:[0,0,1]
	v_mfma_f32_32x32x64_f8f6f4 v[98:113], v[226:233], v[146:153], v[98:113]
	ds_read_b128 v[218:221], v200 offset:49152
	ds_read_b128 v[222:225], v201 offset:49152
	ds_read_b128 v[226:229], v200 offset:55296
	ds_read_b128 v[230:233], v201 offset:55296
	s_waitcnt lgkmcnt(0)
	v_mfma_f32_32x32x64_f8f6f4 v[114:129], v[218:225], v[154:161], v[114:129]
	v_add_f32_e32 v218, v183, v182
	v_add_f32_e32 v218, v184, v218
	v_add_f32_e32 v218, v185, v218
	v_add_f32_e32 v218, v234, v218
	v_add_f32_e32 v218, v235, v218
	v_add_f32_e32 v218, v236, v218
	v_add_f32_e32 v218, v237, v218
	v_add_f32_e32 v218, v238, v218
	v_add_f32_e32 v218, v239, v218
	v_add_f32_e32 v218, v240, v218
	v_add_f32_e32 v218, v241, v218
	v_add_f32_e32 v218, v242, v218
	v_add_f32_e32 v218, v243, v218
	v_add_f32_e32 v218, v244, v218
	v_add_f32_e32 v218, v245, v218
	v_add_f32_e32 v218, v82, v218
	v_add_f32_e32 v218, v83, v218
	v_mfma_f32_32x32x64_f8f6f4 v[98:113], v[226:233], v[154:161], v[98:113]
	v_add_f32_e32 v218, v84, v218
	v_add_f32_e32 v218, v85, v218
	v_add_f32_e32 v218, v86, v218
	v_add_f32_e32 v218, v87, v218
	v_add_f32_e32 v218, v88, v218
	v_add_f32_e32 v218, v89, v218
	v_add_f32_e32 v218, v90, v218
	v_add_f32_e32 v218, v91, v218
	v_add_f32_e32 v218, v92, v218
	v_add_f32_e32 v218, v93, v218
	v_add_f32_e32 v218, v94, v218
	v_add_f32_e32 v218, v95, v218
	v_add_f32_e32 v218, v96, v218
	v_add_f32_e32 v218, v97, v218
	v_mov_b32_e32 v219, v218
	s_nop 1
	v_permlane32_swap_b32_e32 v218, v219
	s_cmp_eq_u32 s94, 0
	s_cbranch_scc0 .Lstg_mid4_l0
	s_waitcnt vmcnt(0)
	s_barrier
	s_mov_b32 m0, s92
	s_nop 0
	global_load_lds_dwordx4 v164, s[24:25]
	s_mov_b32 m0, s86
	s_nop 0
	global_load_lds_dwordx4 v170, s[26:27]
	s_add_u32 s24, s24, 0x3000
	s_addc_u32 s25, s25, 0
	s_add_u32 s26, s26, 64
	s_addc_u32 s27, s27, 0
.Lstg_mid4_l0:
	ds_read_b128 v[86:89], v194 offset:32768
	ds_read_b128 v[82:85], v193 offset:32768
	ds_read_b128 v[90:93], v193 offset:34816
	ds_read_b128 v[94:97], v194 offset:34816
	v_max_f32_e32 v182, v114, v115
	s_waitcnt lgkmcnt(0)
	v_mfma_f32_32x32x64_f8f6f4 v[2:17], v[130:137], v[82:89], v[2:17]
	v_max3_f32 v182, v182, v116, v117
	v_max3_f32 v182, v182, v118, v119
	v_max3_f32 v182, v182, v120, v121
	v_max3_f32 v182, v182, v122, v123
	v_max3_f32 v182, v182, v124, v125
	v_max3_f32 v182, v182, v126, v127
	v_max3_f32 v182, v182, v128, v129
	v_max3_f32 v182, v182, v98, v99
	v_mov_b32_e32 v220, 1.0
	v_mfma_f32_32x32x64_f8f6f4 v[50:65], v[130:137], v[90:97], v[50:65]
	ds_read_b128 v[82:85], v193 offset:36864
	ds_read_b128 v[90:93], v193 offset:38912
	ds_read_b128 v[86:89], v194 offset:36864
	ds_read_b128 v[94:97], v194 offset:38912
	s_waitcnt lgkmcnt(0)
	v_mfma_f32_32x32x64_f8f6f4 v[34:49], v[130:137], v[82:89], v[34:49]
	v_max3_f32 v82, v182, v100, v101
	v_max3_f32 v82, v82, v102, v103
	v_max3_f32 v82, v82, v104, v105
	v_max3_f32 v82, v82, v106, v107
	v_max3_f32 v82, v82, v108, v109
	v_max3_f32 v82, v82, v110, v111
	v_max3_f32 v82, v82, v112, v113
	v_mov_b32_e32 v83, v82
	s_nop 1
	v_permlane32_swap_b32_e32 v82, v83
	v_max_f32_e32 v82, v82, v83
	v_cmp_ge_f32_e32 vcc, s85, v82
	s_cmp_eq_u64 vcc, exec
	v_mfma_f32_32x32x64_f8f6f4 v[18:33], v[130:137], v[90:97], v[18:33]
	s_cbranch_scc0 .LBB0_935
	s_setprio 0
	s_branch .LBB0_922

; __device__ __forceinline__ void finishSM(f32x16& p0, f32x16& p1, float alpha, float& l_reg, v8i& pa) {
; #pragma unroll
;   for (int r = 0; r < 16; ++r) p1[r] = __builtin_amdgcn_exp2f(p1[r]);
;   float ps = 0;
; #pragma unroll
;   for (int r = 0; r < 16; ++r) ps += p0[r];
; #pragma unroll
;   for (int r = 0; r < 16; ++r) ps += p1[r];
;   { auto rr = __builtin_amdgcn_permlane32_swap(__float_as_uint(ps), __float_as_uint(ps), false, false);
;     ps = __uint_as_float(rr[0]) + __uint_as_float(rr[1]); }
;   l_reg = l_reg * alpha + ps;
; #pragma unroll
;   for (int q = 0; q < 4; ++q) { int w0 = pa[q], w1 = pa[4 + q];
;     w0 = __builtin_amdgcn_cvt_pk_fp8_f32(p0[4 * q], p0[4 * q + 1], w0, false); w0 = __builtin_amdgcn_cvt_pk_fp8_f32(p0[4 * q + 2], p0[4 * q + 3], w0, true);
;     w1 = __builtin_amdgcn_cvt_pk_fp8_f32(p1[4 * q], p1[4 * q + 1], w1, false); w1 = __builtin_amdgcn_cvt_pk_fp8_f32(p1[4 * q + 2], p1[4 * q + 3], w1, true);
;     pa[q] = w0; pa[4 + q] = w1; }
; }
; __device__ __forceinline__ void qkt(f32x16& p0, f32x16& p1, const char* Ks, const v8i* qr, int r32, int hi, const f32x16& nm16) {
; #pragma unroll
;   for (int s = 0; s < 3; ++s) { const int c0 = 4 * s + 2 * hi;
;     const v8i a0 = __builtin_shufflevector(*reinterpret_cast<const v4i*>(Ks + k8_off(r32, c0)), *reinterpret_cast<const v4i*>(Ks + k8_off(r32, c0 + 1)), 0, 1, 2, 3, 4, 5, 6, 7);
;     const v8i a1 = __builtin_shufflevector(*reinterpret_cast<const v4i*>(Ks + 32 * DQK + k8_off(r32, c0)), *reinterpret_cast<const v4i*>(Ks + 32 * DQK + k8_off(r32, c0 + 1)), 0, 1, 2, 3, 4, 5, 6, 7);
;     p0 = __builtin_amdgcn_mfma_scale_f32_32x32x64_f8f6f4(a0, qr[s], s == 0 ? nm16 : p0, 0, 0, 0, 0, 0, 0);
;     p1 = __builtin_amdgcn_mfma_scale_f32_32x32x64_f8f6f4(a1, qr[s], s == 0 ? nm16 : p1, 0, 0, 0, 0, 0, 0); }
; }
.Lstg_end4_l0:
	v_exp_f32_e32 v176, v114
	v_exp_f32_e32 v177, v115
	v_exp_f32_e32 v178, v116
	v_exp_f32_e32 v179, v117
	v_exp_f32_e32 v180, v118
	v_exp_f32_e32 v181, v119
	v_exp_f32_e32 v182, v120
	v_exp_f32_e32 v183, v121
	v_exp_f32_e32 v184, v122
	v_exp_f32_e32 v185, v123
	v_exp_f32_e32 v221, v124
	v_exp_f32_e32 v238, v125
	v_exp_f32_e32 v239, v126
	v_exp_f32_e32 v240, v127
	v_exp_f32_e32 v241, v128
	v_exp_f32_e32 v242, v129
	ds_read_b128 v[82:85], v196 offset:8192
	ds_read_b128 v[86:89], v197 offset:8192
	ds_read_b128 v[222:225], v196 offset:14336
	ds_read_b128 v[226:229], v197 offset:14336
	v_exp_f32_e32 v100, v100
	v_exp_f32_e32 v101, v101
	s_waitcnt lgkmcnt(0)
	v_mfma_f32_32x32x64_f8f6f4 v[114:129], v[82:89], v[138:145], v[66:81]
	v_exp_f32_e32 v102, v102
	v_exp_f32_e32 v103, v103
	v_exp_f32_e32 v104, v104
	v_exp_f32_e32 v105, v105
	v_exp_f32_e32 v106, v106
	v_exp_f32_e32 v107, v107
	v_exp_f32_e32 v108, v108
	v_exp_f32_e32 v110, v110
	v_exp_f32_e32 v111, v111
	v_exp_f32_e32 v109, v109
	v_exp_f32_e32 v112, v112
	v_exp_f32_e32 v113, v113
	v_cvt_pk_fp8_f32 v130, v176, v177
	v_cvt_pk_fp8_f32 v131, v180, v181
	v_cvt_pk_fp8_f32 v135, v102, v103
	v_mfma_f32_32x32x64_f8f6f4 v[82:97], v[222:229], v[138:145], v[66:81]
	ds_read_b128 v[222:225], v198 offset:8192
	ds_read_b128 v[226:229], v199 offset:8192
	ds_read_b128 v[230:233], v198 offset:14336
	ds_read_b128 v[234:237], v199 offset:14336
	s_setprio 1
	v_cvt_pk_fp8_f32 v132, v184, v185
	v_cvt_pk_fp8_f32 v136, v106, v107
	v_cvt_pk_fp8_f32 v133, v239, v240
	v_cvt_pk_fp8_f32 v137, v110, v111
	v_cvt_pk_fp8_f32 v130, v178, v179 op_sel:[0,0,1]
	v_cvt_pk_fp8_f32 v131, v182, v183 op_sel:[0,0,1]
	v_cvt_pk_fp8_f32 v135, v104, v105 op_sel:[0,0,1]
	v_cvt_pk_fp8_f32 v132, v221, v238 op_sel:[0,0,1]
	v_cvt_pk_fp8_f32 v136, v108, v109 op_sel:[0,0,1]
	v_cvt_pk_fp8_f32 v133, v241, v242 op_sel:[0,0,1]
	v_cvt_pk_fp8_f32 v137, v112, v113 op_sel:[0,0,1]
	s_waitcnt lgkmcnt(0)
	v_mfma_f32_32x32x64_f8f6f4 v[114:129], v[222:229], v[146:153], v[114:129]
	v_mfma_f32_32x32x64_f8f6f4 v[82:97], v[230:237], v[146:153], v[82:97]
	ds_read_b128 v[222:225], v200 offset:8192
	ds_read_b128 v[226:229], v201 offset:8192
	ds_read_b128 v[230:233], v200 offset:14336
	ds_read_b128 v[234:237], v201 offset:14336
	s_waitcnt lgkmcnt(0)
	v_mfma_f32_32x32x64_f8f6f4 v[114:129], v[222:229], v[154:161], v[114:129]
	v_exp_f32_e32 v222, v98
	v_add_f32_e32 v98, v177, v176
	v_add_f32_e32 v98, v178, v98
	v_add_f32_e32 v98, v179, v98
	v_add_f32_e32 v98, v180, v98
	v_add_f32_e32 v98, v181, v98
	v_add_f32_e32 v98, v182, v98
	v_add_f32_e32 v98, v183, v98
	v_add_f32_e32 v98, v184, v98
	v_add_f32_e32 v98, v185, v98
	v_add_f32_e32 v98, v221, v98
	v_add_f32_e32 v98, v238, v98
	v_add_f32_e32 v98, v239, v98
	v_exp_f32_e32 v223, v99
	v_add_f32_e32 v98, v240, v98
	v_add_f32_e32 v98, v241, v98
	v_add_f32_e32 v98, v242, v98
	v_add_f32_e32 v98, v222, v98
	v_add_f32_e32 v98, v223, v98
	v_mfma_f32_32x32x64_f8f6f4 v[82:97], v[230:237], v[154:161], v[82:97]
	v_add_f32_e32 v98, v100, v98
	v_add_f32_e32 v98, v101, v98
	v_add_f32_e32 v98, v102, v98
	v_add_f32_e32 v98, v103, v98
	v_add_f32_e32 v98, v104, v98
	v_add_f32_e32 v98, v105, v98
	v_add_f32_e32 v98, v106, v98
	v_add_f32_e32 v98, v107, v98
	v_add_f32_e32 v98, v108, v98
	v_cvt_pk_fp8_f32 v134, v222, v223
	v_add_f32_e32 v98, v109, v98
	v_add_f32_e32 v98, v110, v98
	v_add_f32_e32 v98, v111, v98
	v_add_f32_e32 v98, v112, v98
	v_cvt_pk_fp8_f32 v134, v100, v101 op_sel:[0,0,1]
	v_add_f32_e32 v98, v113, v98
	v_mov_b32_e32 v99, v98
	s_nop 1
	v_permlane32_swap_b32_e32 v98, v99
	s_cmp_eq_u32 s94, 0
	s_cbranch_scc0 .Lstg_mid5_l0
	s_waitcnt vmcnt(0)
	s_barrier
	s_cmp_lt_i32 s9, 49
	s_cbranch_scc0 .Lstg_mid5_l0
	s_mov_b32 m0, s90
	s_nop 0
	global_load_lds_dwordx4 v164, s[24:25]
	s_mov_b32 m0, s88
	s_nop 0
	global_load_lds_dwordx4 v170, s[26:27]
	s_add_u32 s24, s24, 0x3000
	s_addc_u32 s25, s25, 0
	s_add_u32 s26, s26, 64
	s_addc_u32 s27, s27, 0

; template <bool FIRST>
; __device__ __forceinline__ void partialSM(f32x16& p0, f32x16& p1, float& m_reg, f32x16& nm16, float& alpha) {
;   float pmax = p0[0];
; #pragma unroll
;   for (int r = 1; r < 16; ++r) pmax = fmaxf(pmax, p0[r]);
; #pragma unroll
;   for (int r = 0; r < 16; ++r) pmax = fmaxf(pmax, p1[r]);
;   { auto rr = __builtin_amdgcn_permlane32_swap(__float_as_uint(pmax), __float_as_uint(pmax), false, false);
;     pmax = fmaxf(__uint_as_float(rr[0]), __uint_as_float(rr[1])); }
;   if (!FIRST && __builtin_expect(__all(pmax <= THR2), 1)) { alpha = 1.f; }
;   else { const float d = FIRST ? pmax : fmaxf(pmax, 0.f);
;     alpha = FIRST ? 1.f : __builtin_amdgcn_exp2f(-d); m_reg += d;
;     const float nm = -m_reg;
; #pragma unroll
;     for (int r = 0; r < 16; ++r) { p0[r] -= d; p1[r] -= d; float t = nm16[r]; asm volatile("v_mov_b32 %0, %1" : "+v"(t) : "v"(nm)); nm16[r] = t; } }
; #pragma unroll
;   for (int r = 0; r < 16; ++r) p0[r] = __builtin_amdgcn_exp2f(p0[r]);
; }
; __device__ __forceinline__ void finishSM(f32x16& p0, f32x16& p1, float alpha, float& l_reg, v8i& pa) {
; #pragma unroll
;   for (int r = 0; r < 16; ++r) p1[r] = __builtin_amdgcn_exp2f(p1[r]);
;   float ps = 0;
; #pragma unroll
;   for (int r = 0; r < 16; ++r) ps += p0[r];
; #pragma unroll
;   for (int r = 0; r < 16; ++r) ps += p1[r];
;   { auto rr = __builtin_amdgcn_permlane32_swap(__float_as_uint(ps), __float_as_uint(ps), false, false);
;     ps = __uint_as_float(rr[0]) + __uint_as_float(rr[1]); }
;   l_reg = l_reg * alpha + ps;
; #pragma unroll
;   for (int q = 0; q < 4; ++q) { int w0 = pa[q], w1 = pa[4 + q];
;     w0 = __builtin_amdgcn_cvt_pk_fp8_f32(p0[4 * q], p0[4 * q + 1], w0, false); w0 = __builtin_amdgcn_cvt_pk_fp8_f32(p0[4 * q + 2], p0[4 * q + 3], w0, true);
;     w1 = __builtin_amdgcn_cvt_pk_fp8_f32(p1[4 * q], p1[4 * q + 1], w1, false); w1 = __builtin_amdgcn_cvt_pk_fp8_f32(p1[4 * q + 2], p1[4 * q + 3], w1, true);
;     pa[q] = w0; pa[4 + q] = w1; }
; }
; __device__ __forceinline__ void qkt(f32x16& p0, f32x16& p1, const char* Ks, const v8i* qr, int r32, int hi, const f32x16& nm16) {
; #pragma unroll
;   for (int s = 0; s < 3; ++s) { const int c0 = 4 * s + 2 * hi;
;     const v8i a0 = __builtin_shufflevector(*reinterpret_cast<const v4i*>(Ks + k8_off(r32, c0)), *reinterpret_cast<const v4i*>(Ks + k8_off(r32, c0 + 1)), 0, 1, 2, 3, 4, 5, 6, 7);
.LBB0_939:
	v_lshl_add_u64 v[98:99], v[168:169], 0, s[56:57]
	s_mov_b32 m0, s89
	s_nop 0
	global_load_lds_dwordx4 v[98:99], off
	s_mov_b32 m0, s88
	s_nop 0
	global_load_lds_dwordx4 v170, s[26:27]
	ds_read_b128 v[102:105], v197 offset:20480
	ds_read_b128 v[98:101], v196 offset:20480
	ds_read_b128 v[202:205], v196 offset:26624
	ds_read_b128 v[206:209], v197 offset:26624
	ds_read_b128 v[210:213], v198 offset:20480
	ds_read_b128 v[238:241], v198 offset:26624
	ds_read_b128 v[214:217], v199 offset:20480
	ds_read_b128 v[242:245], v199 offset:26624
	ds_read_b128 v[246:249], v200 offset:20480
	ds_read_b128 v[178:181], v200 offset:26624
	ds_read_b128 v[250:253], v201 offset:20480
	ds_read_b128 v[182:185], v201 offset:26624
	s_waitcnt lgkmcnt(0)
	v_mfma_f32_32x32x64_f8f6f4 v[114:129], v[98:105], v[138:145], v[66:81]
	v_add_f32_e32 v170, v236, v235
	v_add_f32_e32 v170, v233, v170
	v_add_f32_e32 v170, v234, v170
	v_add_f32_e32 v170, v231, v170
	v_add_f32_e32 v170, v232, v170
	v_add_f32_e32 v170, v229, v170
	v_add_f32_e32 v170, v230, v170
	v_add_f32_e32 v170, v227, v170
	v_add_f32_e32 v170, v228, v170
	v_add_f32_e32 v170, v225, v170
	v_add_f32_e32 v170, v226, v170
	v_exp_f32_e32 v82, v82
	v_add_f32_e32 v170, v223, v170
	v_exp_f32_e32 v83, v83
	v_add_f32_e32 v170, v224, v170
	v_mfma_f32_32x32x64_f8f6f4 v[98:113], v[202:209], v[138:145], v[66:81]
	v_exp_f32_e32 v84, v84
	v_add_f32_e32 v170, v221, v170
	v_exp_f32_e32 v85, v85
	v_add_f32_e32 v170, v222, v170
	v_exp_f32_e32 v86, v86
	v_add_f32_e32 v170, v82, v170
	v_exp_f32_e32 v87, v87
	v_add_f32_e32 v170, v83, v170
	v_exp_f32_e32 v88, v88
	v_add_f32_e32 v170, v84, v170
	v_exp_f32_e32 v89, v89
	v_add_f32_e32 v170, v85, v170
	v_exp_f32_e32 v90, v90
	v_add_f32_e32 v170, v86, v170
	v_exp_f32_e32 v91, v91
	v_mfma_f32_32x32x64_f8f6f4 v[114:129], v[210:217], v[146:153], v[114:129]
	v_add_f32_e32 v170, v87, v170
	v_exp_f32_e32 v92, v92
	v_exp_f32_e32 v94, v94
	v_exp_f32_e32 v95, v95
	v_add_f32_e32 v170, v88, v170
	v_exp_f32_e32 v93, v93
	v_add_f32_e32 v170, v89, v170
	v_add_f32_e32 v170, v90, v170
	v_add_f32_e32 v170, v91, v170
	v_exp_f32_e32 v96, v96
	v_exp_f32_e32 v97, v97
	v_add_f32_e32 v170, v92, v170
	v_cvt_pk_fp8_f32 v130, v235, v236
	v_cvt_pk_fp8_f32 v134, v82, v83
	v_cvt_pk_fp8_f32 v131, v231, v232
	v_mfma_f32_32x32x64_f8f6f4 v[98:113], v[238:245], v[146:153], v[98:113]
	v_cvt_pk_fp8_f32 v135, v86, v87
	v_cvt_pk_fp8_f32 v132, v227, v228
	v_cvt_pk_fp8_f32 v136, v90, v91
	v_cvt_pk_fp8_f32 v133, v223, v224
	v_cvt_pk_fp8_f32 v137, v94, v95
	v_add_f32_e32 v170, v93, v170
	v_add_f32_e32 v170, v94, v170
	v_add_f32_e32 v170, v95, v170
	v_add_f32_e32 v170, v96, v170
	v_cvt_pk_fp8_f32 v130, v233, v234 op_sel:[0,0,1]
	v_cvt_pk_fp8_f32 v134, v84, v85 op_sel:[0,0,1]
	v_cvt_pk_fp8_f32 v131, v229, v230 op_sel:[0,0,1]
	v_cvt_pk_fp8_f32 v135, v88, v89 op_sel:[0,0,1]
	v_cvt_pk_fp8_f32 v132, v225, v226 op_sel:[0,0,1]
	v_cvt_pk_fp8_f32 v136, v92, v93 op_sel:[0,0,1]
	v_mfma_f32_32x32x64_f8f6f4 v[114:129], v[246:253], v[154:161], v[114:129]
	v_cvt_pk_fp8_f32 v133, v221, v222 op_sel:[0,0,1]
	v_cvt_pk_fp8_f32 v137, v96, v97 op_sel:[0,0,1]
	v_add_f32_e32 v170, v97, v170
	v_mov_b32_e32 v171, v170
	s_nop 1
	v_permlane32_swap_b32_e32 v170, v171
	v_mfma_f32_32x32x64_f8f6f4 v[98:113], v[178:185], v[154:161], v[98:113]
	ds_read_b128 v[86:89], v194
	ds_read_b128 v[82:85], v193
	ds_read_b128 v[90:93], v193 offset:2048
	ds_read_b128 v[94:97], v194 offset:2048
	s_nop 7
	v_max_f32_e32 v172, v114, v115
	v_max_f32_e32 v173, v114, v114
	s_waitcnt lgkmcnt(0)
	v_mfma_f32_32x32x64_f8f6f4 v[2:17], v[130:137], v[82:89], v[2:17]
	v_max3_f32 v172, v172, v116, v117
	v_max3_f32 v172, v172, v118, v119
	v_max3_f32 v172, v172, v120, v121
	v_max3_f32 v172, v172, v122, v123
	v_max3_f32 v172, v172, v124, v125
	v_max3_f32 v172, v172, v126, v127
	v_max3_f32 v172, v172, v128, v129
	v_max3_f32 v172, v172, v98, v99
	v_mfma_f32_32x32x64_f8f6f4 v[50:65], v[130:137], v[90:97], v[50:65]
	ds_read_b128 v[82:85], v193 offset:4096
	ds_read_b128 v[90:93], v193 offset:6144
	ds_read_b128 v[86:89], v194 offset:4096
	ds_read_b128 v[94:97], v194 offset:6144
	s_waitcnt lgkmcnt(0)
	v_mfma_f32_32x32x64_f8f6f4 v[34:49], v[130:137], v[82:89], v[34:49]
	v_max3_f32 v82, v172, v100, v101
	v_max3_f32 v82, v82, v102, v103
	v_max3_f32 v82, v82, v104, v105
	v_max3_f32 v82, v82, v106, v107
	v_max3_f32 v82, v82, v108, v109
	v_max3_f32 v82, v82, v110, v111
	v_max3_f32 v82, v82, v112, v113
	v_mov_b32_e32 v83, v82
	s_nop 1
	v_permlane32_swap_b32_e32 v82, v83
	v_max_f32_e32 v82, v82, v83
	v_cmp_ge_f32_e32 vcc, s85, v82
	s_cmp_eq_u64 vcc, exec
	v_mfma_f32_32x32x64_f8f6f4 v[18:33], v[130:137], v[90:97], v[18:33]
	v_mov_b32_e32 v172, 1.0
	s_cbranch_scc0 .LBB0_1086
	s_branch .LBB0_944

; template <bool FIRST>
; __device__ __forceinline__ void partialSM(f32x16& p0, f32x16& p1, float& m_reg, f32x16& nm16, float& alpha) {
;   float pmax = p0[0];
; #pragma unroll
;   for (int r = 1; r < 16; ++r) pmax = fmaxf(pmax, p0[r]);
; #pragma unroll
;   for (int r = 0; r < 16; ++r) pmax = fmaxf(pmax, p1[r]);
;   { auto rr = __builtin_amdgcn_permlane32_swap(__float_as_uint(pmax), __float_as_uint(pmax), false, false);
;     pmax = fmaxf(__uint_as_float(rr[0]), __uint_as_float(rr[1])); }
;   if (!FIRST && __builtin_expect(__all(pmax <= THR2), 1)) { alpha = 1.f; }
;   else { const float d = FIRST ? pmax : fmaxf(pmax, 0.f);
;     alpha = FIRST ? 1.f : __builtin_amdgcn_exp2f(-d); m_reg += d;
;     const float nm = -m_reg;
; #pragma unroll
;     for (int r = 0; r < 16; ++r) { p0[r] -= d; p1[r] -= d; float t = nm16[r]; asm volatile("v_mov_b32 %0, %1" : "+v"(t) : "v"(nm)); nm16[r] = t; } }
; #pragma unroll
;   for (int r = 0; r < 16; ++r) p0[r] = __builtin_amdgcn_exp2f(p0[r]);
; }
; __device__ __forceinline__ void finishSM(f32x16& p0, f32x16& p1, float alpha, float& l_reg, v8i& pa) {
; #pragma unroll
;   for (int r = 0; r < 16; ++r) p1[r] = __builtin_amdgcn_exp2f(p1[r]);
;   float ps = 0;
; #pragma unroll
;   for (int r = 0; r < 16; ++r) ps += p0[r];
; #pragma unroll
;   for (int r = 0; r < 16; ++r) ps += p1[r];
;   { auto rr = __builtin_amdgcn_permlane32_swap(__float_as_uint(ps), __float_as_uint(ps), false, false);
;     ps = __uint_as_float(rr[0]) + __uint_as_float(rr[1]); }
;   l_reg = l_reg * alpha + ps;
; #pragma unroll
;   for (int q = 0; q < 4; ++q) { int w0 = pa[q], w1 = pa[4 + q];
;     w0 = __builtin_amdgcn_cvt_pk_fp8_f32(p0[4 * q], p0[4 * q + 1], w0, false); w0 = __builtin_amdgcn_cvt_pk_fp8_f32(p0[4 * q + 2], p0[4 * q + 3], w0, true);
;     w1 = __builtin_amdgcn_cvt_pk_fp8_f32(p1[4 * q], p1[4 * q + 1], w1, false); w1 = __builtin_amdgcn_cvt_pk_fp8_f32(p1[4 * q + 2], p1[4 * q + 3], w1, true);
;     pa[q] = w0; pa[4 + q] = w1; }
; }
; __device__ __forceinline__ void qkt(f32x16& p0, f32x16& p1, const char* Ks, const v8i* qr, int r32, int hi, const f32x16& nm16) {
; #pragma unroll
;   for (int s = 0; s < 3; ++s) { const int c0 = 4 * s + 2 * hi;
;     const v8i a0 = __builtin_shufflevector(*reinterpret_cast<const v4i*>(Ks + k8_off(r32, c0)), *reinterpret_cast<const v4i*>(Ks + k8_off(r32, c0 + 1)), 0, 1, 2, 3, 4, 5, 6, 7);
.LBB0_946:
	s_mov_b32 m0, s86
	v_lshl_add_u64 v[82:83], v[168:169], 0, s[58:59]
	global_load_lds_dwordx4 v[82:83], off
	v_exp_f32_e32 v166, v114
	v_exp_f32_e32 v167, v115
	v_exp_f32_e32 v168, v116
	v_exp_f32_e32 v169, v117
	v_exp_f32_e32 v173, v118
	v_exp_f32_e32 v174, v119
	v_exp_f32_e32 v175, v120
	v_exp_f32_e32 v177, v121
	v_exp_f32_e32 v234, v122
	v_exp_f32_e32 v235, v123
	v_exp_f32_e32 v236, v124
	v_exp_f32_e32 v237, v125
	v_exp_f32_e32 v238, v126
	v_exp_f32_e32 v239, v127
	v_exp_f32_e32 v240, v128
	v_exp_f32_e32 v241, v129
	ds_read_b128 v[86:89], v197 offset:49152
	ds_read_b128 v[82:85], v196 offset:49152
	ds_read_b128 v[178:181], v196 offset:55296
	ds_read_b128 v[182:185], v197 offset:55296
	ds_read_b128 v[202:205], v198 offset:49152
	ds_read_b128 v[210:213], v198 offset:55296
	ds_read_b128 v[206:209], v199 offset:49152
	ds_read_b128 v[214:217], v199 offset:55296
	ds_read_b128 v[218:221], v200 offset:49152
	ds_read_b128 v[226:229], v200 offset:55296
	ds_read_b128 v[222:225], v201 offset:49152
	ds_read_b128 v[230:233], v201 offset:55296
	s_waitcnt lgkmcnt(0)
	v_mfma_f32_32x32x64_f8f6f4 v[114:129], v[82:89], v[138:145], v[66:81]
	v_add_f32_e32 v164, v167, v166
	v_add_f32_e32 v164, v168, v164
	v_add_f32_e32 v164, v169, v164
	v_add_f32_e32 v164, v173, v164
	v_add_f32_e32 v164, v174, v164
	v_add_f32_e32 v164, v175, v164
	v_add_f32_e32 v164, v177, v164
	v_add_f32_e32 v164, v234, v164
	v_add_f32_e32 v164, v235, v164
	v_add_f32_e32 v164, v236, v164
	v_add_f32_e32 v164, v237, v164
	v_exp_f32_e32 v98, v98
	v_add_f32_e32 v164, v238, v164
	v_exp_f32_e32 v99, v99
	v_add_f32_e32 v164, v239, v164
	v_mfma_f32_32x32x64_f8f6f4 v[82:97], v[178:185], v[138:145], v[66:81]
	v_exp_f32_e32 v100, v100
	v_add_f32_e32 v164, v240, v164
	v_exp_f32_e32 v101, v101
	v_add_f32_e32 v164, v241, v164
	v_exp_f32_e32 v102, v102
	v_add_f32_e32 v164, v98, v164
	v_exp_f32_e32 v103, v103
	v_add_f32_e32 v164, v99, v164
	v_exp_f32_e32 v104, v104
	v_add_f32_e32 v164, v100, v164
	v_exp_f32_e32 v105, v105
	v_add_f32_e32 v164, v101, v164
	v_exp_f32_e32 v106, v106
	v_add_f32_e32 v164, v102, v164
	v_exp_f32_e32 v107, v107
	v_mfma_f32_32x32x64_f8f6f4 v[114:129], v[202:209], v[146:153], v[114:129]
	v_add_f32_e32 v164, v103, v164
	v_exp_f32_e32 v108, v108
	v_exp_f32_e32 v110, v110
	v_exp_f32_e32 v111, v111
	v_add_f32_e32 v164, v104, v164
	v_exp_f32_e32 v109, v109
	v_add_f32_e32 v164, v105, v164
	v_add_f32_e32 v164, v106, v164
	v_add_f32_e32 v164, v107, v164
	v_exp_f32_e32 v112, v112
	v_exp_f32_e32 v113, v113
	v_add_f32_e32 v164, v108, v164
	v_cvt_pk_fp8_f32 v130, v166, v167
	v_cvt_pk_fp8_f32 v134, v98, v99
	v_cvt_pk_fp8_f32 v131, v173, v174
	v_mfma_f32_32x32x64_f8f6f4 v[82:97], v[210:217], v[146:153], v[82:97]
	v_cvt_pk_fp8_f32 v135, v102, v103
	v_cvt_pk_fp8_f32 v132, v234, v235
	v_cvt_pk_fp8_f32 v136, v106, v107
	v_cvt_pk_fp8_f32 v133, v238, v239
	v_cvt_pk_fp8_f32 v137, v110, v111
	v_add_f32_e32 v164, v109, v164
	v_add_f32_e32 v164, v110, v164
	v_add_f32_e32 v164, v111, v164
	v_add_f32_e32 v164, v112, v164
	v_cvt_pk_fp8_f32 v130, v168, v169 op_sel:[0,0,1]
	v_cvt_pk_fp8_f32 v134, v100, v101 op_sel:[0,0,1]
	v_cvt_pk_fp8_f32 v131, v175, v177 op_sel:[0,0,1]
	v_cvt_pk_fp8_f32 v135, v104, v105 op_sel:[0,0,1]
	v_cvt_pk_fp8_f32 v132, v236, v237 op_sel:[0,0,1]
	v_cvt_pk_fp8_f32 v136, v108, v109 op_sel:[0,0,1]
	v_mfma_f32_32x32x64_f8f6f4 v[114:129], v[218:225], v[154:161], v[114:129]
	v_cvt_pk_fp8_f32 v133, v240, v241 op_sel:[0,0,1]
	v_cvt_pk_fp8_f32 v137, v112, v113 op_sel:[0,0,1]
	v_add_f32_e32 v164, v113, v164
	v_mov_b32_e32 v165, v164
	s_nop 1
	v_permlane32_swap_b32_e32 v164, v165
	v_mfma_f32_32x32x64_f8f6f4 v[82:97], v[226:233], v[154:161], v[82:97]
	ds_read_b128 v[102:105], v194 offset:32768
	ds_read_b128 v[98:101], v193 offset:32768
	ds_read_b128 v[106:109], v193 offset:34816
	ds_read_b128 v[110:113], v194 offset:34816
	s_nop 7
	v_max_f32_e32 v166, v114, v115
	v_max_f32_e32 v167, v114, v114
	s_waitcnt lgkmcnt(0)
	v_mfma_f32_32x32x64_f8f6f4 v[2:17], v[130:137], v[98:105], v[2:17]
	v_max3_f32 v166, v166, v116, v117
	v_max3_f32 v166, v166, v118, v119
	v_max3_f32 v166, v166, v120, v121
	v_max3_f32 v166, v166, v122, v123
	v_max3_f32 v166, v166, v124, v125
	v_max3_f32 v166, v166, v126, v127
	v_max3_f32 v166, v166, v128, v129
	v_max3_f32 v166, v166, v82, v83
	v_mfma_f32_32x32x64_f8f6f4 v[50:65], v[130:137], v[106:113], v[50:65]
	ds_read_b128 v[98:101], v193 offset:36864
	ds_read_b128 v[106:109], v193 offset:38912
	ds_read_b128 v[102:105], v194 offset:36864
	ds_read_b128 v[110:113], v194 offset:38912
	s_waitcnt lgkmcnt(0)
	v_mfma_f32_32x32x64_f8f6f4 v[34:49], v[130:137], v[98:105], v[34:49]
	v_max3_f32 v98, v166, v84, v85
	v_max3_f32 v98, v98, v86, v87
	v_max3_f32 v98, v98, v88, v89
	v_max3_f32 v98, v98, v90, v91
	v_max3_f32 v98, v98, v92, v93
	v_max3_f32 v98, v98, v94, v95
	v_max3_f32 v98, v98, v96, v97
	v_mov_b32_e32 v99, v98
	s_nop 1
	v_permlane32_swap_b32_e32 v98, v99
	v_max_f32_e32 v98, v98, v99
	v_cmp_ge_f32_e32 vcc, s85, v98
	s_cmp_eq_u64 vcc, exec
	v_mfma_f32_32x32x64_f8f6f4 v[18:33], v[130:137], v[106:113], v[18:33]
	v_mov_b32_e32 v166, 1.0
	s_cbranch_scc0 .LBB0_1087
	s_branch .LBB0_951

; template <bool FIRST>
; __device__ __forceinline__ void partialSM(f32x16& p0, f32x16& p1, float& m_reg, f32x16& nm16, float& alpha) {
;   float pmax = p0[0];
; #pragma unroll
;   for (int r = 1; r < 16; ++r) pmax = fmaxf(pmax, p0[r]);
; #pragma unroll
;   for (int r = 0; r < 16; ++r) pmax = fmaxf(pmax, p1[r]);
;   { auto rr = __builtin_amdgcn_permlane32_swap(__float_as_uint(pmax), __float_as_uint(pmax), false, false);
;     pmax = fmaxf(__uint_as_float(rr[0]), __uint_as_float(rr[1])); }
;   if (!FIRST && __builtin_expect(__all(pmax <= THR2), 1)) { alpha = 1.f; }
;   else { const float d = FIRST ? pmax : fmaxf(pmax, 0.f);
;     alpha = FIRST ? 1.f : __builtin_amdgcn_exp2f(-d); m_reg += d;
;     const float nm = -m_reg;
; #pragma unroll
;     for (int r = 0; r < 16; ++r) { p0[r] -= d; p1[r] -= d; float t = nm16[r]; asm volatile("v_mov_b32 %0, %1" : "+v"(t) : "v"(nm)); nm16[r] = t; } }
; #pragma unroll
;   for (int r = 0; r < 16; ++r) p0[r] = __builtin_amdgcn_exp2f(p0[r]);
; }
; __device__ __forceinline__ void finishSM(f32x16& p0, f32x16& p1, float alpha, float& l_reg, v8i& pa) {
; #pragma unroll
;   for (int r = 0; r < 16; ++r) p1[r] = __builtin_amdgcn_exp2f(p1[r]);
;   float ps = 0;
; #pragma unroll
;   for (int r = 0; r < 16; ++r) ps += p0[r];
; #pragma unroll
;   for (int r = 0; r < 16; ++r) ps += p1[r];
;   { auto rr = __builtin_amdgcn_permlane32_swap(__float_as_uint(ps), __float_as_uint(ps), false, false);
;     ps = __uint_as_float(rr[0]) + __uint_as_float(rr[1]); }
;   l_reg = l_reg * alpha + ps;
; #pragma unroll
;   for (int q = 0; q < 4; ++q) { int w0 = pa[q], w1 = pa[4 + q];
;     w0 = __builtin_amdgcn_cvt_pk_fp8_f32(p0[4 * q], p0[4 * q + 1], w0, false); w0 = __builtin_amdgcn_cvt_pk_fp8_f32(p0[4 * q + 2], p0[4 * q + 3], w0, true);
;     w1 = __builtin_amdgcn_cvt_pk_fp8_f32(p1[4 * q], p1[4 * q + 1], w1, false); w1 = __builtin_amdgcn_cvt_pk_fp8_f32(p1[4 * q + 2], p1[4 * q + 3], w1, true);
;     pa[q] = w0; pa[4 + q] = w1; }
; }
; __device__ __forceinline__ void qkt(f32x16& p0, f32x16& p1, const char* Ks, const v8i* qr, int r32, int hi, const f32x16& nm16) {
; #pragma unroll
;   for (int s = 0; s < 3; ++s) { const int c0 = 4 * s + 2 * hi;
;     const v8i a0 = __builtin_shufflevector(*reinterpret_cast<const v4i*>(Ks + k8_off(r32, c0)), *reinterpret_cast<const v4i*>(Ks + k8_off(r32, c0 + 1)), 0, 1, 2, 3, 4, 5, 6, 7);
.LBB0_951:
	s_waitcnt vmcnt(0)
	s_barrier
	v_exp_f32_e32 v167, v114
	v_exp_f32_e32 v168, v115
	v_exp_f32_e32 v169, v116
	v_exp_f32_e32 v173, v117
	v_exp_f32_e32 v174, v118
	v_exp_f32_e32 v175, v119
	v_exp_f32_e32 v177, v120
	v_exp_f32_e32 v234, v121
	v_exp_f32_e32 v235, v122
	v_exp_f32_e32 v236, v123
	v_exp_f32_e32 v237, v124
	v_exp_f32_e32 v238, v125
	v_exp_f32_e32 v239, v126
	v_exp_f32_e32 v240, v127
	v_exp_f32_e32 v241, v128
	v_exp_f32_e32 v242, v129
	ds_read_b128 v[118:121], v197 offset:8192
	ds_read_b128 v[114:117], v196 offset:8192
	ds_read_b128 v[178:181], v196 offset:14336
	ds_read_b128 v[182:185], v197 offset:14336
	v_exp_f32_e32 v196, v82
	s_waitcnt lgkmcnt(0)
	v_mfma_f32_32x32x64_f8f6f4 v[98:113], v[114:121], v[138:145], v[66:81]
	ds_read_b128 v[202:205], v198 offset:8192
	ds_read_b128 v[210:213], v198 offset:14336
	ds_read_b128 v[206:209], v199 offset:8192
	ds_read_b128 v[214:217], v199 offset:14336
	ds_read_b128 v[218:221], v200 offset:8192
	ds_read_b128 v[226:229], v200 offset:14336
	ds_read_b128 v[222:225], v201 offset:8192
	ds_read_b128 v[230:233], v201 offset:14336
	v_add_f32_e32 v82, v168, v167
	v_add_f32_e32 v82, v169, v82
	v_add_f32_e32 v82, v173, v82
	v_add_f32_e32 v82, v174, v82
	v_add_f32_e32 v82, v175, v82
	v_add_f32_e32 v82, v177, v82
	v_add_f32_e32 v82, v234, v82
	v_add_f32_e32 v82, v235, v82
	v_add_f32_e32 v82, v236, v82
	v_add_f32_e32 v82, v237, v82
	v_add_f32_e32 v82, v238, v82
	v_add_f32_e32 v82, v239, v82
	v_exp_f32_e32 v197, v83
	v_add_f32_e32 v82, v240, v82
	v_mfma_f32_32x32x64_f8f6f4 v[114:129], v[178:185], v[138:145], v[66:81]
	v_exp_f32_e32 v84, v84
	v_add_f32_e32 v82, v241, v82
	v_exp_f32_e32 v85, v85
	v_add_f32_e32 v82, v242, v82
	v_exp_f32_e32 v86, v86
	v_add_f32_e32 v82, v196, v82
	v_exp_f32_e32 v87, v87
	v_add_f32_e32 v82, v197, v82
	v_exp_f32_e32 v88, v88
	v_add_f32_e32 v82, v84, v82
	v_exp_f32_e32 v89, v89
	v_add_f32_e32 v82, v85, v82
	v_exp_f32_e32 v90, v90
	v_add_f32_e32 v82, v86, v82
	v_exp_f32_e32 v91, v91
	s_waitcnt lgkmcnt(0)
	v_mfma_f32_32x32x64_f8f6f4 v[98:113], v[202:209], v[146:153], v[98:113]
	v_add_f32_e32 v82, v87, v82
	v_exp_f32_e32 v92, v92
	v_exp_f32_e32 v94, v94
	v_exp_f32_e32 v95, v95
	v_add_f32_e32 v82, v88, v82
	v_exp_f32_e32 v93, v93
	v_add_f32_e32 v82, v89, v82
	v_add_f32_e32 v82, v90, v82
	v_add_f32_e32 v82, v91, v82
	v_exp_f32_e32 v96, v96
	v_exp_f32_e32 v97, v97
	v_add_f32_e32 v82, v92, v82
	v_cvt_pk_fp8_f32 v130, v167, v168
	v_cvt_pk_fp8_f32 v134, v196, v197
	v_cvt_pk_fp8_f32 v131, v174, v175
	v_mfma_f32_32x32x64_f8f6f4 v[114:129], v[210:217], v[146:153], v[114:129]
	v_cvt_pk_fp8_f32 v135, v86, v87
	v_cvt_pk_fp8_f32 v132, v235, v236
	v_cvt_pk_fp8_f32 v136, v90, v91
	v_cvt_pk_fp8_f32 v133, v239, v240
	v_cvt_pk_fp8_f32 v137, v94, v95
	v_add_f32_e32 v82, v93, v82
	v_add_f32_e32 v82, v94, v82
	v_add_f32_e32 v82, v95, v82
	v_add_f32_e32 v82, v96, v82
	v_cvt_pk_fp8_f32 v130, v169, v173 op_sel:[0,0,1]
	v_cvt_pk_fp8_f32 v134, v84, v85 op_sel:[0,0,1]
	v_cvt_pk_fp8_f32 v131, v177, v234 op_sel:[0,0,1]
	v_cvt_pk_fp8_f32 v135, v88, v89 op_sel:[0,0,1]
	v_cvt_pk_fp8_f32 v132, v237, v238 op_sel:[0,0,1]
	v_cvt_pk_fp8_f32 v136, v92, v93 op_sel:[0,0,1]
	v_mfma_f32_32x32x64_f8f6f4 v[98:113], v[218:225], v[154:161], v[98:113]
	v_cvt_pk_fp8_f32 v133, v241, v242 op_sel:[0,0,1]
	v_cvt_pk_fp8_f32 v137, v96, v97 op_sel:[0,0,1]
	v_add_f32_e32 v82, v97, v82
	v_mov_b32_e32 v83, v82
	s_nop 1
	v_permlane32_swap_b32_e32 v82, v83
	v_mfma_f32_32x32x64_f8f6f4 v[114:129], v[226:233], v[154:161], v[114:129]
	ds_read_b128 v[88:91], v194 offset:40960
	ds_read_b128 v[84:87], v193 offset:40960
	ds_read_b128 v[138:141], v193 offset:43008
	ds_read_b128 v[142:145], v194 offset:43008
	s_nop 7
	v_max_f32_e32 v92, v98, v99
	v_max_f32_e32 v93, v98, v98
	s_waitcnt lgkmcnt(0)
	v_mfma_f32_32x32x64_f8f6f4 v[2:17], v[130:137], v[84:91], v[2:17]
	v_max3_f32 v92, v92, v100, v101
	v_max3_f32 v92, v92, v102, v103
	v_max3_f32 v92, v92, v104, v105
	v_max3_f32 v92, v92, v106, v107
	v_max3_f32 v92, v92, v108, v109
	v_max3_f32 v92, v92, v110, v111
	v_max3_f32 v92, v92, v112, v113
	v_max3_f32 v92, v92, v114, v115
	v_mfma_f32_32x32x64_f8f6f4 v[50:65], v[130:137], v[138:145], v[50:65]
	ds_read_b128 v[84:87], v193 offset:45056
	ds_read_b128 v[138:141], v193 offset:47104
	ds_read_b128 v[88:91], v194 offset:45056
	ds_read_b128 v[142:145], v194 offset:47104
	s_waitcnt lgkmcnt(0)
	v_mfma_f32_32x32x64_f8f6f4 v[34:49], v[130:137], v[84:91], v[34:49]
	v_max3_f32 v84, v92, v116, v117
	v_max3_f32 v84, v84, v118, v119
	v_max3_f32 v84, v84, v120, v121
	v_max3_f32 v84, v84, v122, v123
	v_max3_f32 v84, v84, v124, v125
	v_max3_f32 v84, v84, v126, v127
	v_max3_f32 v84, v84, v128, v129
	v_mov_b32_e32 v85, v84
	s_nop 1
	v_permlane32_swap_b32_e32 v84, v85
	v_max_f32_e32 v85, v84, v85
	v_cmp_ge_f32_e32 vcc, s85, v85
	s_cmp_eq_u64 vcc, exec
	v_mfma_f32_32x32x64_f8f6f4 v[18:33], v[130:137], v[138:145], v[18:33]
	v_mov_b32_e32 v84, 1.0
	s_cbranch_scc0 .LBB0_1088
	s_branch .LBB0_956

; __device__ __forceinline__ void finishSM(f32x16& p0, f32x16& p1, float alpha, float& l_reg, v8i& pa) {
; #pragma unroll
;   for (int r = 0; r < 16; ++r) p1[r] = __builtin_amdgcn_exp2f(p1[r]);
;   float ps = 0;
; #pragma unroll
;   for (int r = 0; r < 16; ++r) ps += p0[r];
; #pragma unroll
;   for (int r = 0; r < 16; ++r) ps += p1[r];
;   { auto rr = __builtin_amdgcn_permlane32_swap(__float_as_uint(ps), __float_as_uint(ps), false, false);
;     ps = __uint_as_float(rr[0]) + __uint_as_float(rr[1]); }
;   l_reg = l_reg * alpha + ps;
; #pragma unroll
;   for (int q = 0; q < 4; ++q) { int w0 = pa[q], w1 = pa[4 + q];
;     w0 = __builtin_amdgcn_cvt_pk_fp8_f32(p0[4 * q], p0[4 * q + 1], w0, false); w0 = __builtin_amdgcn_cvt_pk_fp8_f32(p0[4 * q + 2], p0[4 * q + 3], w0, true);
;     w1 = __builtin_amdgcn_cvt_pk_fp8_f32(p1[4 * q], p1[4 * q + 1], w1, false); w1 = __builtin_amdgcn_cvt_pk_fp8_f32(p1[4 * q + 2], p1[4 * q + 3], w1, true);
;     pa[q] = w0; pa[4 + q] = w1; }
; }
; __device__ __forceinline__ void qkt(f32x16& p0, f32x16& p1, const char* Ks, const v8i* qr, int r32, int hi, const f32x16& nm16) {
; #pragma unroll
;   for (int s = 0; s < 3; ++s) { const int c0 = 4 * s + 2 * hi;
;     const v8i a0 = __builtin_shufflevector(*reinterpret_cast<const v4i*>(Ks + k8_off(r32, c0)), *reinterpret_cast<const v4i*>(Ks + k8_off(r32, c0 + 1)), 0, 1, 2, 3, 4, 5, 6, 7);
;     const v8i a1 = __builtin_shufflevector(*reinterpret_cast<const v4i*>(Ks + 32 * DQK + k8_off(r32, c0)), *reinterpret_cast<const v4i*>(Ks + 32 * DQK + k8_off(r32, c0 + 1)), 0, 1, 2, 3, 4, 5, 6, 7);
;     p0 = __builtin_amdgcn_mfma_scale_f32_32x32x64_f8f6f4(a0, qr[s], s == 0 ? nm16 : p0, 0, 0, 0, 0, 0, 0);
;     p1 = __builtin_amdgcn_mfma_scale_f32_32x32x64_f8f6f4(a1, qr[s], s == 0 ? nm16 : p1, 0, 0, 0, 0, 0, 0); }
; }
; __device__ __forceinline__ void pv_d0(f32x16* o, const char* Vs, v8i pa, int r32, int hi) {
; #pragma unroll
;   for (int d0 = 0; d0 < 4; ++d0) { const int row = 32 * d0 + r32, x = (row >> 2) & 3;
;     const v8i vb = __builtin_shufflevector(*reinterpret_cast<const v4i*>(Vs + row * 64 + (((2 * hi) ^ x) << 4)), *reinterpret_cast<const v4i*>(Vs + row * 64 + (((2 * hi + 1) ^ x) << 4)), 0, 1, 2, 3, 4, 5, 6, 7);
;     o[d0] = __builtin_amdgcn_mfma_scale_f32_32x32x64_f8f6f4(pa, vb, o[d0], 0, 0, 0, 0, 0, 0); }
; }
.LBB0_956:
	v_exp_f32_e32 v67, v98
	v_exp_f32_e32 v68, v99
	v_exp_f32_e32 v69, v100
	v_exp_f32_e32 v70, v101
	v_exp_f32_e32 v71, v102
	v_exp_f32_e32 v72, v103
	v_add_f32_e32 v66, v68, v67
	v_exp_f32_e32 v73, v104
	v_add_f32_e32 v66, v69, v66
	v_exp_f32_e32 v74, v105
	v_add_f32_e32 v66, v70, v66
	v_exp_f32_e32 v75, v106
	v_add_f32_e32 v66, v71, v66
	v_exp_f32_e32 v76, v107
	v_add_f32_e32 v66, v72, v66
	v_exp_f32_e32 v77, v108
	v_add_f32_e32 v66, v73, v66
	v_exp_f32_e32 v78, v109
	v_add_f32_e32 v66, v74, v66
	v_exp_f32_e32 v79, v110
	v_add_f32_e32 v66, v75, v66
	v_exp_f32_e32 v80, v111
	v_add_f32_e32 v66, v76, v66
	v_exp_f32_e32 v81, v112
	v_add_f32_e32 v66, v77, v66
	v_exp_f32_e32 v85, v113
	v_add_f32_e32 v66, v78, v66
	v_exp_f32_e32 v86, v114
	v_add_f32_e32 v66, v79, v66
	v_exp_f32_e32 v87, v115
	v_add_f32_e32 v66, v80, v66
	v_exp_f32_e32 v88, v116
	v_add_f32_e32 v66, v81, v66
	v_exp_f32_e32 v89, v117
	v_add_f32_e32 v66, v85, v66
	v_exp_f32_e32 v90, v118
	v_add_f32_e32 v66, v86, v66
	v_exp_f32_e32 v91, v119
	v_add_f32_e32 v66, v87, v66
	v_exp_f32_e32 v92, v120
	v_add_f32_e32 v66, v88, v66
	v_exp_f32_e32 v93, v121
	v_add_f32_e32 v66, v89, v66
	v_exp_f32_e32 v94, v122
	v_add_f32_e32 v66, v90, v66
	v_exp_f32_e32 v95, v123
	v_add_f32_e32 v66, v91, v66
	v_exp_f32_e32 v96, v124
	v_add_f32_e32 v66, v92, v66
	v_exp_f32_e32 v97, v125
	v_add_f32_e32 v66, v93, v66
	v_exp_f32_e32 v98, v126
	v_add_f32_e32 v66, v94, v66
	v_exp_f32_e32 v99, v127
	v_add_f32_e32 v66, v95, v66
	v_exp_f32_e32 v100, v128
	v_add_f32_e32 v66, v96, v66
	v_exp_f32_e32 v101, v129
	v_add_f32_e32 v66, v97, v66
	v_add_f32_e32 v66, v98, v66
	v_add_f32_e32 v66, v99, v66
	s_waitcnt vmcnt(0)
	v_add_f32_e32 v66, v100, v66
	v_cvt_pk_fp8_f32 v130, v67, v68
	v_cvt_pk_fp8_f32 v134, v86, v87
	v_cvt_pk_fp8_f32 v131, v71, v72
	v_cvt_pk_fp8_f32 v135, v90, v91
	v_cvt_pk_fp8_f32 v132, v75, v76
	v_cvt_pk_fp8_f32 v136, v94, v95
	v_cvt_pk_fp8_f32 v133, v79, v80
	v_cvt_pk_fp8_f32 v137, v98, v99
	s_barrier
	v_add_f32_e32 v66, v101, v66
	v_mov_b32_e32 v67, v66
	s_nop 1
	v_permlane32_swap_b32_e32 v66, v67
	v_cvt_pk_fp8_f32 v130, v69, v70 op_sel:[0,0,1]
	v_cvt_pk_fp8_f32 v134, v88, v89 op_sel:[0,0,1]
	v_cvt_pk_fp8_f32 v131, v73, v74 op_sel:[0,0,1]
	v_cvt_pk_fp8_f32 v135, v92, v93 op_sel:[0,0,1]
	v_cvt_pk_fp8_f32 v132, v77, v78 op_sel:[0,0,1]
	v_cvt_pk_fp8_f32 v136, v96, v97 op_sel:[0,0,1]
	v_cvt_pk_fp8_f32 v133, v81, v85 op_sel:[0,0,1]
	v_cvt_pk_fp8_f32 v137, v100, v101 op_sel:[0,0,1]
	ds_read_b128 v[72:75], v194
	ds_read_b128 v[68:71], v193
	ds_read_b128 v[86:89], v193 offset:2048
	ds_read_b128 v[90:93], v194 offset:2048
	s_waitcnt lgkmcnt(0)
	v_mfma_f32_32x32x64_f8f6f4 v[2:17], v[130:137], v[68:75], v[2:17]
	v_mfma_f32_32x32x64_f8f6f4 v[50:65], v[130:137], v[86:93], v[50:65]
	ds_read_b128 v[72:75], v194 offset:4096
	ds_read_b128 v[68:71], v193 offset:4096
	ds_read_b128 v[86:89], v193 offset:6144
	ds_read_b128 v[90:93], v194 offset:6144
	s_waitcnt lgkmcnt(0)
	v_mfma_f32_32x32x64_f8f6f4 v[34:49], v[130:137], v[68:75], v[34:49]
	v_mfma_f32_32x32x64_f8f6f4 v[18:33], v[130:137], v[86:93], v[18:33]
	s_and_saveexec_b64 s[0:1], s[2:3]
	s_cbranch_execz .LBB0_958
	v_add_f32_e32 v68, v170, v171
	v_fmac_f32_e32 v68, v162, v176
	v_add_f32_e32 v69, v164, v165
	v_fmac_f32_e32 v69, v68, v172
	v_add_f32_e32 v68, v82, v83
	v_fmac_f32_e32 v68, v69, v166
	v_add_f32_e32 v66, v66, v67
	v_fmac_f32_e32 v66, v68, v84
	ds_write_b32 v192, v66 offset:61440

; __device__ __forceinline__ void finishSM(f32x16& p0, f32x16& p1, float alpha, float& l_reg, v8i& pa) {
; #pragma unroll
;   for (int r = 0; r < 16; ++r) p1[r] = __builtin_amdgcn_exp2f(p1[r]);
;   float ps = 0;
; #pragma unroll
;   for (int r = 0; r < 16; ++r) ps += p0[r];
; #pragma unroll
;   for (int r = 0; r < 16; ++r) ps += p1[r];
;   { auto rr = __builtin_amdgcn_permlane32_swap(__float_as_uint(ps), __float_as_uint(ps), false, false);
;     ps = __uint_as_float(rr[0]) + __uint_as_float(rr[1]); }
;   l_reg = l_reg * alpha + ps;
; #pragma unroll
;   for (int q = 0; q < 4; ++q) { int w0 = pa[q], w1 = pa[4 + q];
;     w0 = __builtin_amdgcn_cvt_pk_fp8_f32(p0[4 * q], p0[4 * q + 1], w0, false); w0 = __builtin_amdgcn_cvt_pk_fp8_f32(p0[4 * q + 2], p0[4 * q + 3], w0, true);
;     w1 = __builtin_amdgcn_cvt_pk_fp8_f32(p1[4 * q], p1[4 * q + 1], w1, false); w1 = __builtin_amdgcn_cvt_pk_fp8_f32(p1[4 * q + 2], p1[4 * q + 3], w1, true);
;     pa[q] = w0; pa[4 + q] = w1; }
; }
; __device__ __forceinline__ void qkt(f32x16& p0, f32x16& p1, const char* Ks, const v8i* qr, int r32, int hi, const f32x16& nm16) {
; #pragma unroll
;   for (int s = 0; s < 3; ++s) { const int c0 = 4 * s + 2 * hi;
;     const v8i a0 = __builtin_shufflevector(*reinterpret_cast<const v4i*>(Ks + k8_off(r32, c0)), *reinterpret_cast<const v4i*>(Ks + k8_off(r32, c0 + 1)), 0, 1, 2, 3, 4, 5, 6, 7);
;     const v8i a1 = __builtin_shufflevector(*reinterpret_cast<const v4i*>(Ks + 32 * DQK + k8_off(r32, c0)), *reinterpret_cast<const v4i*>(Ks + 32 * DQK + k8_off(r32, c0 + 1)), 0, 1, 2, 3, 4, 5, 6, 7);
;     p0 = __builtin_amdgcn_mfma_scale_f32_32x32x64_f8f6f4(a0, qr[s], s == 0 ? nm16 : p0, 0, 0, 0, 0, 0, 0);
;     p1 = __builtin_amdgcn_mfma_scale_f32_32x32x64_f8f6f4(a1, qr[s], s == 0 ? nm16 : p1, 0, 0, 0, 0, 0, 0); }
; }
.Lstg_end4_l1:
	v_exp_f32_e32 v176, v114
	v_exp_f32_e32 v177, v115
	v_exp_f32_e32 v178, v116
	v_exp_f32_e32 v179, v117
	v_exp_f32_e32 v180, v118
	v_exp_f32_e32 v181, v119
	v_exp_f32_e32 v182, v120
	v_exp_f32_e32 v183, v121
	v_exp_f32_e32 v184, v122
	v_exp_f32_e32 v185, v123
	v_exp_f32_e32 v221, v124
	v_exp_f32_e32 v238, v125
	v_exp_f32_e32 v239, v126
	v_exp_f32_e32 v240, v127
	v_exp_f32_e32 v241, v128
	v_exp_f32_e32 v242, v129
	ds_read_b128 v[82:85], v196 offset:8192
	ds_read_b128 v[86:89], v197 offset:8192
	ds_read_b128 v[222:225], v196 offset:14336
	ds_read_b128 v[226:229], v197 offset:14336
	v_exp_f32_e32 v100, v100
	v_exp_f32_e32 v101, v101
	s_waitcnt lgkmcnt(0)
	v_mfma_f32_32x32x64_f8f6f4 v[114:129], v[82:89], v[138:145], v[66:81]
	v_exp_f32_e32 v102, v102
	v_exp_f32_e32 v103, v103
	v_exp_f32_e32 v104, v104
	v_exp_f32_e32 v105, v105
	v_exp_f32_e32 v106, v106
	v_exp_f32_e32 v107, v107
	v_exp_f32_e32 v108, v108
	v_exp_f32_e32 v110, v110
	v_exp_f32_e32 v111, v111
	v_exp_f32_e32 v109, v109
	v_exp_f32_e32 v112, v112
	v_exp_f32_e32 v113, v113
	v_cvt_pk_fp8_f32 v130, v176, v177
	v_cvt_pk_fp8_f32 v131, v180, v181
	v_cvt_pk_fp8_f32 v135, v102, v103
	v_mfma_f32_32x32x64_f8f6f4 v[82:97], v[222:229], v[138:145], v[66:81]
	ds_read_b128 v[222:225], v198 offset:8192
	ds_read_b128 v[226:229], v199 offset:8192
	ds_read_b128 v[230:233], v198 offset:14336
	ds_read_b128 v[234:237], v199 offset:14336
	s_setprio 1
	v_cvt_pk_fp8_f32 v132, v184, v185
	v_cvt_pk_fp8_f32 v136, v106, v107
	v_cvt_pk_fp8_f32 v133, v239, v240
	v_cvt_pk_fp8_f32 v137, v110, v111
	v_cvt_pk_fp8_f32 v130, v178, v179 op_sel:[0,0,1]
	v_cvt_pk_fp8_f32 v131, v182, v183 op_sel:[0,0,1]
	v_cvt_pk_fp8_f32 v135, v104, v105 op_sel:[0,0,1]
	v_cvt_pk_fp8_f32 v132, v221, v238 op_sel:[0,0,1]
	v_cvt_pk_fp8_f32 v136, v108, v109 op_sel:[0,0,1]
	v_cvt_pk_fp8_f32 v133, v241, v242 op_sel:[0,0,1]
	v_cvt_pk_fp8_f32 v137, v112, v113 op_sel:[0,0,1]
	s_waitcnt lgkmcnt(0)
	v_mfma_f32_32x32x64_f8f6f4 v[114:129], v[222:229], v[146:153], v[114:129]
	v_mfma_f32_32x32x64_f8f6f4 v[82:97], v[230:237], v[146:153], v[82:97]
	ds_read_b128 v[222:225], v200 offset:8192
	ds_read_b128 v[226:229], v201 offset:8192
	ds_read_b128 v[230:233], v200 offset:14336
	ds_read_b128 v[234:237], v201 offset:14336
	s_waitcnt lgkmcnt(0)
	v_mfma_f32_32x32x64_f8f6f4 v[114:129], v[222:229], v[154:161], v[114:129]
	v_exp_f32_e32 v222, v98
	v_add_f32_e32 v98, v177, v176
	v_add_f32_e32 v98, v178, v98
	v_add_f32_e32 v98, v179, v98
	v_add_f32_e32 v98, v180, v98
	v_add_f32_e32 v98, v181, v98
	v_add_f32_e32 v98, v182, v98
	v_add_f32_e32 v98, v183, v98
	v_add_f32_e32 v98, v184, v98
	v_add_f32_e32 v98, v185, v98
	v_add_f32_e32 v98, v221, v98
	v_add_f32_e32 v98, v238, v98
	v_add_f32_e32 v98, v239, v98
	v_exp_f32_e32 v223, v99
	v_add_f32_e32 v98, v240, v98
	v_add_f32_e32 v98, v241, v98
	v_add_f32_e32 v98, v242, v98
	v_add_f32_e32 v98, v222, v98
	v_add_f32_e32 v98, v223, v98
	v_mfma_f32_32x32x64_f8f6f4 v[82:97], v[230:237], v[154:161], v[82:97]
	v_add_f32_e32 v98, v100, v98
	v_add_f32_e32 v98, v101, v98
	v_add_f32_e32 v98, v102, v98
	v_add_f32_e32 v98, v103, v98
	v_add_f32_e32 v98, v104, v98
	v_add_f32_e32 v98, v105, v98
	v_add_f32_e32 v98, v106, v98
	v_add_f32_e32 v98, v107, v98
	v_add_f32_e32 v98, v108, v98
	v_cvt_pk_fp8_f32 v134, v222, v223
	v_add_f32_e32 v98, v109, v98
	v_add_f32_e32 v98, v110, v98
	v_add_f32_e32 v98, v111, v98
	v_add_f32_e32 v98, v112, v98
	v_cvt_pk_fp8_f32 v134, v100, v101 op_sel:[0,0,1]
	v_add_f32_e32 v98, v113, v98
	v_mov_b32_e32 v99, v98
	s_nop 1
	v_permlane32_swap_b32_e32 v98, v99
	s_cmp_eq_u32 s94, 0
	s_cbranch_scc0 .Lstg_mid5_l1
	s_waitcnt vmcnt(0)
	s_barrier
	s_cmp_lt_i32 s8, 49
	s_cbranch_scc0 .Lstg_mid5_l1
	s_mov_b32 m0, s90
	s_nop 0
	global_load_lds_dwordx4 v164, s[24:25]
	s_mov_b32 m0, s88
	s_nop 0
	global_load_lds_dwordx4 v170, s[26:27]
	s_add_u32 s24, s24, 0x3000
	s_addc_u32 s25, s25, 0
	s_add_u32 s26, s26, 64
	s_addc_u32 s27, s27, 0
